# gate/up GEMM SwiGLU epilogue re-emitted with packed f32 VALU (v_pk_fma/mul/add_f32), same per-element operation order (bit-identical), 578 instead of ~860 instructions per unit; on top of previous sta
# speedup vs baseline: 1.0084x; 1.0084x over previous
; __device__ __forceinline__ unsigned pk4_fp8(float a, float b, float c, float d) { int w = __builtin_amdgcn_cvt_pk_fp8_f32(a, b, 0, false); w = __builtin_amdgcn_cvt_pk_fp8_f32(c, d, w, true); return (unsigned)w; }
;     __device__ __forceinline__ void operator()(const f32x4 (&acc)[2][2][4][2], const Unit& u, int wr, int wc, int fr, int fq) const {
;         const int row0 = u.pm * BM + wr * 64 + fr, c0 = u.pn * HALF + wc * 32 + 8 * fq;
;         const float* bp = bgu + (size_t)u.aux * 2048 + c0;
;         const f32x4 bg0 = *(const f32x4*)(bp), bg1 = *(const f32x4*)(bp + 4), bu0 = *(const f32x4*)(bp + 1024), bu1 = *(const f32x4*)(bp + 1028);
; #pragma unroll
;         for (int ai = 0; ai < 2; ++ai)
; #pragma unroll
;             for (int mp = 0; mp < 2; ++mp) {
;                 u32x2 wq[2];
; #pragma unroll
;                 for (int mi = 0; mi < 2; ++mi) { const int m = 2 * mp + mi;
;                     const f32x4 g0 = acc[ai][0][m][0] * ascale + bg0, g1 = acc[ai][0][m][1] * ascale + bg1, u0 = acc[ai][1][m][0] * ascale + bu0, u1 = acc[ai][1][m][1] * ascale + bu1;
;                     float r[8];
; #pragma unroll
;                     for (int j = 0; j < 4; ++j) {
;                         float gg = fminf(g0[j], 7.f), uu = fminf(fmaxf(u0[j], -7.f), 7.f); r[j] = 4.f * (uu + 1.f) * gg * __builtin_amdgcn_rcpf(1.f + __expf(-1.702f * gg));
;                         gg = fminf(g1[j], 7.f); uu = fminf(fmaxf(u1[j], -7.f), 7.f); r[4 + j] = 4.f * (uu + 1.f) * gg * __builtin_amdgcn_rcpf(1.f + __expf(-1.702f * gg));
;                     }
;                     wq[mi].x = pk4_fp8(r[0], r[1], r[2], r[3]); wq[mi].y = pk4_fp8(r[4], r[5], r[6], r[7]); }
;                 *(u32x4*)(act + (size_t)(row0 + ai * HALF + (2 * mp + (fq & 1)) * 16) * EFF + (c0 - 8 * (fq & 1))) = widen16(wq[0], wq[1]);
.LBB0_1433:
	v_mov_b32_e32 v18, v192
	s_lshl_b32 s36, s36, 7
	v_lshrrev_b32_e32 v0, 1, v18
	s_ashr_i32 s39, s38, 31
	s_lshl_b32 s40, s77, 8
	v_and_or_b32 v0, v0, 24, s36
	s_lshl_b64 s[38:39], s[38:39], 13
	v_or_b32_e32 v16, s64, v0
	s_add_u32 s38, s4, s38
	s_addc_u32 s39, s5, s39
	v_ashrrev_i32_e32 v17, 31, v16
	v_lshl_add_u64 v[0:1], v[16:17], 2, s[38:39]
	global_load_dwordx4 v[12:15], v[0:1], off
	global_load_dwordx4 v[4:7], v[0:1], off offset:16
	v_add_co_u32_e32 v2, vcc, s73, v0
	v_bfe_u32 v17, v18, 4, 1
	s_nop 0
	v_addc_co_u32_e32 v3, vcc, 0, v1, vcc
	v_lshl_add_u64 v[0:1], v[0:1], 0, s[20:21]
	global_load_dwordx4 v[8:11], v[2:3], off
	v_lshlrev_b32_e32 v19, 3, v17
	global_load_dwordx4 v[0:3], v[0:1], off offset:16
	v_sub_u32_e32 v16, v16, v19
	s_add_i32 s40, s40, s63
	v_and_or_b32 v18, v18, 15, s40
	v_lshl_or_b32 v18, v17, 4, v18
	v_ashrrev_i32_e32 v17, 31, v16
	s_andn2_b64 vcc, exec, s[26:27]
	s_mov_b64 s[26:27], -1
	s_waitcnt vmcnt(0)
	s_mov_b32 s98, 0x3a000000
	s_mov_b32 s99, 0xbfd9db23
	s_mov_b32 s100, 0x3fb8aa3b
	s_mov_b32 s101, 0
	v_ashrrev_i32_e32 v19, 31, v18
	v_lshlrev_b64 v[48:49], 10, v[18:19]
	v_lshl_add_u64 v[48:49], s[12:13], 0, v[48:49]
	v_lshl_add_u64 v[48:49], v[48:49], 0, v[16:17]
	v_mov_b32_e32 v52, 0x8000
	v_mov_b32_e32 v53, 0
	v_mov_b32_e32 v54, 0x20000
	v_mov_b32_e32 v55, 0
	v_pk_fma_f32 v[24:25], v[188:189], s[98:99], v[12:13] op_sel_hi:[1,0,1]
	v_pk_fma_f32 v[26:27], v[190:191], s[98:99], v[14:15] op_sel_hi:[1,0,1]
	v_pk_fma_f32 v[28:29], v[184:185], s[98:99], v[4:5] op_sel_hi:[1,0,1]
	v_pk_fma_f32 v[30:31], v[186:187], s[98:99], v[6:7] op_sel_hi:[1,0,1]
	v_pk_fma_f32 v[40:41], v[180:181], s[98:99], v[8:9] op_sel_hi:[1,0,1]
	v_pk_fma_f32 v[42:43], v[182:183], s[98:99], v[10:11] op_sel_hi:[1,0,1]
	v_pk_fma_f32 v[44:45], v[176:177], s[98:99], v[0:1] op_sel_hi:[1,0,1]
	v_pk_fma_f32 v[46:47], v[178:179], s[98:99], v[2:3] op_sel_hi:[1,0,1]
	v_min_f32_e32 v24, 0x40e00000, v24
	v_min_f32_e32 v25, 0x40e00000, v25
	v_min_f32_e32 v26, 0x40e00000, v26
	v_min_f32_e32 v27, 0x40e00000, v27
	v_min_f32_e32 v28, 0x40e00000, v28
	v_min_f32_e32 v29, 0x40e00000, v29
	v_min_f32_e32 v30, 0x40e00000, v30
	v_min_f32_e32 v31, 0x40e00000, v31
	v_med3_f32 v40, v40, s74, v203
	v_med3_f32 v41, v41, s74, v203
	v_med3_f32 v42, v42, s74, v203
	v_med3_f32 v43, v43, s74, v203
	v_med3_f32 v44, v44, s74, v203
	v_med3_f32 v45, v45, s74, v203
	v_med3_f32 v46, v46, s74, v203
	v_med3_f32 v47, v47, s74, v203
	v_pk_mul_f32 v[32:33], v[24:25], s[98:99] op_sel:[0,1] op_sel_hi:[1,1]
	v_pk_mul_f32 v[34:35], v[26:27], s[98:99] op_sel:[0,1] op_sel_hi:[1,1]
	v_pk_mul_f32 v[36:37], v[28:29], s[98:99] op_sel:[0,1] op_sel_hi:[1,1]
	v_pk_mul_f32 v[38:39], v[30:31], s[98:99] op_sel:[0,1] op_sel_hi:[1,1]
	v_pk_mul_f32 v[32:33], v[32:33], s[100:101] op_sel_hi:[1,0]
	v_pk_mul_f32 v[34:35], v[34:35], s[100:101] op_sel_hi:[1,0]
	v_pk_mul_f32 v[36:37], v[36:37], s[100:101] op_sel_hi:[1,0]
	v_pk_mul_f32 v[38:39], v[38:39], s[100:101] op_sel_hi:[1,0]
	v_pk_fma_f32 v[40:41], v[40:41], 4.0, 4.0 op_sel_hi:[1,0,0]
	v_pk_fma_f32 v[42:43], v[42:43], 4.0, 4.0 op_sel_hi:[1,0,0]
	v_pk_fma_f32 v[44:45], v[44:45], 4.0, 4.0 op_sel_hi:[1,0,0]
	v_pk_fma_f32 v[46:47], v[46:47], 4.0, 4.0 op_sel_hi:[1,0,0]
	v_exp_f32_e32 v32, v32
	v_exp_f32_e32 v33, v33
	v_exp_f32_e32 v34, v34
	v_exp_f32_e32 v35, v35
	v_exp_f32_e32 v36, v36
	v_exp_f32_e32 v37, v37
	v_exp_f32_e32 v38, v38
	v_exp_f32_e32 v39, v39
	v_pk_mul_f32 v[40:41], v[24:25], v[40:41]
	v_pk_mul_f32 v[42:43], v[26:27], v[42:43]
	v_pk_mul_f32 v[44:45], v[28:29], v[44:45]
	v_pk_mul_f32 v[46:47], v[30:31], v[46:47]
	v_pk_add_f32 v[32:33], v[32:33], 1.0 op_sel_hi:[1,0]
	v_pk_add_f32 v[34:35], v[34:35], 1.0 op_sel_hi:[1,0]
	v_pk_add_f32 v[36:37], v[36:37], 1.0 op_sel_hi:[1,0]
	v_pk_add_f32 v[38:39], v[38:39], 1.0 op_sel_hi:[1,0]
	v_rcp_f32_e32 v32, v32
	v_rcp_f32_e32 v33, v33
	v_rcp_f32_e32 v34, v34
	v_rcp_f32_e32 v35, v35
	v_rcp_f32_e32 v36, v36
	v_rcp_f32_e32 v37, v37
	v_rcp_f32_e32 v38, v38
	v_rcp_f32_e32 v39, v39
	v_pk_mul_f32 v[40:41], v[32:33], v[40:41]
	v_pk_mul_f32 v[42:43], v[34:35], v[42:43]
	v_pk_mul_f32 v[44:45], v[36:37], v[44:45]
	v_pk_mul_f32 v[46:47], v[38:39], v[46:47]
	v_cvt_pk_fp8_f32 v20, v40, v41
	v_cvt_pk_fp8_f32 v21, v44, v45
	v_cvt_pk_fp8_f32 v20, v42, v43 op_sel:[0,0,1]
	v_cvt_pk_fp8_f32 v21, v46, v47 op_sel:[0,0,1]
	v_pk_fma_f32 v[24:25], v[172:173], s[98:99], v[12:13] op_sel_hi:[1,0,1]
	v_pk_fma_f32 v[26:27], v[174:175], s[98:99], v[14:15] op_sel_hi:[1,0,1]
	v_pk_fma_f32 v[28:29], v[168:169], s[98:99], v[4:5] op_sel_hi:[1,0,1]
	v_pk_fma_f32 v[30:31], v[170:171], s[98:99], v[6:7] op_sel_hi:[1,0,1]
	v_pk_fma_f32 v[40:41], v[164:165], s[98:99], v[8:9] op_sel_hi:[1,0,1]
	v_pk_fma_f32 v[42:43], v[166:167], s[98:99], v[10:11] op_sel_hi:[1,0,1]
	v_pk_fma_f32 v[44:45], v[160:161], s[98:99], v[0:1] op_sel_hi:[1,0,1]
	v_pk_fma_f32 v[46:47], v[162:163], s[98:99], v[2:3] op_sel_hi:[1,0,1]
	v_min_f32_e32 v24, 0x40e00000, v24
	v_min_f32_e32 v25, 0x40e00000, v25
	v_min_f32_e32 v26, 0x40e00000, v26
	v_min_f32_e32 v27, 0x40e00000, v27
	v_min_f32_e32 v28, 0x40e00000, v28
	v_min_f32_e32 v29, 0x40e00000, v29
	v_min_f32_e32 v30, 0x40e00000, v30
	v_min_f32_e32 v31, 0x40e00000, v31
	v_med3_f32 v40, v40, s74, v203
	v_med3_f32 v41, v41, s74, v203
	v_med3_f32 v42, v42, s74, v203
	v_med3_f32 v43, v43, s74, v203
	v_med3_f32 v44, v44, s74, v203
	v_med3_f32 v45, v45, s74, v203
	v_med3_f32 v46, v46, s74, v203
	v_med3_f32 v47, v47, s74, v203
	v_pk_mul_f32 v[32:33], v[24:25], s[98:99] op_sel:[0,1] op_sel_hi:[1,1]
	v_pk_mul_f32 v[34:35], v[26:27], s[98:99] op_sel:[0,1] op_sel_hi:[1,1]
	v_pk_mul_f32 v[36:37], v[28:29], s[98:99] op_sel:[0,1] op_sel_hi:[1,1]
; __device__ __forceinline__ unsigned pk4_fp8(float a, float b, float c, float d) { int w = __builtin_amdgcn_cvt_pk_fp8_f32(a, b, 0, false); w = __builtin_amdgcn_cvt_pk_fp8_f32(c, d, w, true); return (unsigned)w; }
;     __device__ __forceinline__ void operator()(const f32x4 (&acc)[2][2][4][2], const Unit& u, int wr, int wc, int fr, int fq) const {
;     ...
;                 for (int mi = 0; mi < 2; ++mi) { const int m = 2 * mp + mi;
;                     const f32x4 g0 = acc[ai][0][m][0] * ascale + bg0, g1 = acc[ai][0][m][1] * ascale + bg1, u0 = acc[ai][1][m][0] * ascale + bu0, u1 = acc[ai][1][m][1] * ascale + bu1;
;                     float r[8];
; #pragma unroll
;                     for (int j = 0; j < 4; ++j) {
;                         float gg = fminf(g0[j], 7.f), uu = fminf(fmaxf(u0[j], -7.f), 7.f); r[j] = 4.f * (uu + 1.f) * gg * __builtin_amdgcn_rcpf(1.f + __expf(-1.702f * gg));
;                         gg = fminf(g1[j], 7.f); uu = fminf(fmaxf(u1[j], -7.f), 7.f); r[4 + j] = 4.f * (uu + 1.f) * gg * __builtin_amdgcn_rcpf(1.f + __expf(-1.702f * gg));
;                     }
;                     wq[mi].x = pk4_fp8(r[0], r[1], r[2], r[3]); wq[mi].y = pk4_fp8(r[4], r[5], r[6], r[7]); }
;                 *(u32x4*)(act + (size_t)(row0 + ai * HALF + (2 * mp + (fq & 1)) * 16) * EFF + (c0 - 8 * (fq & 1))) = widen16(wq[0], wq[1]);
	v_pk_mul_f32 v[38:39], v[30:31], s[98:99] op_sel:[0,1] op_sel_hi:[1,1]
	v_pk_mul_f32 v[32:33], v[32:33], s[100:101] op_sel_hi:[1,0]
	v_pk_mul_f32 v[34:35], v[34:35], s[100:101] op_sel_hi:[1,0]
	v_pk_mul_f32 v[36:37], v[36:37], s[100:101] op_sel_hi:[1,0]
	v_pk_mul_f32 v[38:39], v[38:39], s[100:101] op_sel_hi:[1,0]
	v_pk_fma_f32 v[40:41], v[40:41], 4.0, 4.0 op_sel_hi:[1,0,0]
	v_pk_fma_f32 v[42:43], v[42:43], 4.0, 4.0 op_sel_hi:[1,0,0]
	v_pk_fma_f32 v[44:45], v[44:45], 4.0, 4.0 op_sel_hi:[1,0,0]
	v_pk_fma_f32 v[46:47], v[46:47], 4.0, 4.0 op_sel_hi:[1,0,0]
	v_exp_f32_e32 v32, v32
	v_exp_f32_e32 v33, v33
	v_exp_f32_e32 v34, v34
	v_exp_f32_e32 v35, v35
	v_exp_f32_e32 v36, v36
	v_exp_f32_e32 v37, v37
	v_exp_f32_e32 v38, v38
	v_exp_f32_e32 v39, v39
	v_pk_mul_f32 v[40:41], v[24:25], v[40:41]
	v_pk_mul_f32 v[42:43], v[26:27], v[42:43]
	v_pk_mul_f32 v[44:45], v[28:29], v[44:45]
	v_pk_mul_f32 v[46:47], v[30:31], v[46:47]
	v_pk_add_f32 v[32:33], v[32:33], 1.0 op_sel_hi:[1,0]
	v_pk_add_f32 v[34:35], v[34:35], 1.0 op_sel_hi:[1,0]
	v_pk_add_f32 v[36:37], v[36:37], 1.0 op_sel_hi:[1,0]
	v_pk_add_f32 v[38:39], v[38:39], 1.0 op_sel_hi:[1,0]
	v_rcp_f32_e32 v32, v32
	v_rcp_f32_e32 v33, v33
	v_rcp_f32_e32 v34, v34
	v_rcp_f32_e32 v35, v35
	v_rcp_f32_e32 v36, v36
	v_rcp_f32_e32 v37, v37
	v_rcp_f32_e32 v38, v38
	v_rcp_f32_e32 v39, v39
	v_pk_mul_f32 v[40:41], v[32:33], v[40:41]
	v_pk_mul_f32 v[42:43], v[34:35], v[42:43]
	v_pk_mul_f32 v[44:45], v[36:37], v[44:45]
	v_pk_mul_f32 v[46:47], v[38:39], v[46:47]
	v_cvt_pk_fp8_f32 v22, v40, v41
	v_cvt_pk_fp8_f32 v23, v44, v45
	v_cvt_pk_fp8_f32 v22, v42, v43 op_sel:[0,0,1]
	v_cvt_pk_fp8_f32 v23, v46, v47 op_sel:[0,0,1]
	v_mov_b64_e32 v[50:51], v[48:49]
	s_nop 1
	v_permlane16_swap_b32_e32 v20, v22
	v_permlane16_swap_b32_e32 v21, v23
	global_store_dwordx4 v[50:51], v[20:23], off
	v_pk_fma_f32 v[24:25], v[156:157], s[98:99], v[12:13] op_sel_hi:[1,0,1]
	v_pk_fma_f32 v[26:27], v[158:159], s[98:99], v[14:15] op_sel_hi:[1,0,1]
	v_pk_fma_f32 v[28:29], v[152:153], s[98:99], v[4:5] op_sel_hi:[1,0,1]
	v_pk_fma_f32 v[30:31], v[154:155], s[98:99], v[6:7] op_sel_hi:[1,0,1]
	v_pk_fma_f32 v[40:41], v[148:149], s[98:99], v[8:9] op_sel_hi:[1,0,1]
	v_pk_fma_f32 v[42:43], v[150:151], s[98:99], v[10:11] op_sel_hi:[1,0,1]
	v_pk_fma_f32 v[44:45], v[144:145], s[98:99], v[0:1] op_sel_hi:[1,0,1]
	v_pk_fma_f32 v[46:47], v[146:147], s[98:99], v[2:3] op_sel_hi:[1,0,1]
	v_min_f32_e32 v24, 0x40e00000, v24
	v_min_f32_e32 v25, 0x40e00000, v25
	v_min_f32_e32 v26, 0x40e00000, v26
	v_min_f32_e32 v27, 0x40e00000, v27
	v_min_f32_e32 v28, 0x40e00000, v28
	v_min_f32_e32 v29, 0x40e00000, v29
	v_min_f32_e32 v30, 0x40e00000, v30
	v_min_f32_e32 v31, 0x40e00000, v31
	v_med3_f32 v40, v40, s74, v203
	v_med3_f32 v41, v41, s74, v203
	v_med3_f32 v42, v42, s74, v203
	v_med3_f32 v43, v43, s74, v203
	v_med3_f32 v44, v44, s74, v203
	v_med3_f32 v45, v45, s74, v203
	v_med3_f32 v46, v46, s74, v203
	v_med3_f32 v47, v47, s74, v203
	v_pk_mul_f32 v[32:33], v[24:25], s[98:99] op_sel:[0,1] op_sel_hi:[1,1]
	v_pk_mul_f32 v[34:35], v[26:27], s[98:99] op_sel:[0,1] op_sel_hi:[1,1]
	v_pk_mul_f32 v[36:37], v[28:29], s[98:99] op_sel:[0,1] op_sel_hi:[1,1]
	v_pk_mul_f32 v[38:39], v[30:31], s[98:99] op_sel:[0,1] op_sel_hi:[1,1]
	v_pk_mul_f32 v[32:33], v[32:33], s[100:101] op_sel_hi:[1,0]
	v_pk_mul_f32 v[34:35], v[34:35], s[100:101] op_sel_hi:[1,0]
	v_pk_mul_f32 v[36:37], v[36:37], s[100:101] op_sel_hi:[1,0]
	v_pk_mul_f32 v[38:39], v[38:39], s[100:101] op_sel_hi:[1,0]
	v_pk_fma_f32 v[40:41], v[40:41], 4.0, 4.0 op_sel_hi:[1,0,0]
	v_pk_fma_f32 v[42:43], v[42:43], 4.0, 4.0 op_sel_hi:[1,0,0]
	v_pk_fma_f32 v[44:45], v[44:45], 4.0, 4.0 op_sel_hi:[1,0,0]
	v_pk_fma_f32 v[46:47], v[46:47], 4.0, 4.0 op_sel_hi:[1,0,0]
	v_exp_f32_e32 v32, v32
	v_exp_f32_e32 v33, v33
	v_exp_f32_e32 v34, v34
	v_exp_f32_e32 v35, v35
	v_exp_f32_e32 v36, v36
	v_exp_f32_e32 v37, v37
	v_exp_f32_e32 v38, v38
	v_exp_f32_e32 v39, v39
	v_pk_mul_f32 v[40:41], v[24:25], v[40:41]
	v_pk_mul_f32 v[42:43], v[26:27], v[42:43]
	v_pk_mul_f32 v[44:45], v[28:29], v[44:45]
	v_pk_mul_f32 v[46:47], v[30:31], v[46:47]
	v_pk_add_f32 v[32:33], v[32:33], 1.0 op_sel_hi:[1,0]
	v_pk_add_f32 v[34:35], v[34:35], 1.0 op_sel_hi:[1,0]
	v_pk_add_f32 v[36:37], v[36:37], 1.0 op_sel_hi:[1,0]
	v_pk_add_f32 v[38:39], v[38:39], 1.0 op_sel_hi:[1,0]
	v_rcp_f32_e32 v32, v32
	v_rcp_f32_e32 v33, v33
	v_rcp_f32_e32 v34, v34
	v_rcp_f32_e32 v35, v35
	v_rcp_f32_e32 v36, v36
	v_rcp_f32_e32 v37, v37
	v_rcp_f32_e32 v38, v38
	v_rcp_f32_e32 v39, v39
	v_pk_mul_f32 v[40:41], v[32:33], v[40:41]
	v_pk_mul_f32 v[42:43], v[34:35], v[42:43]
	v_pk_mul_f32 v[44:45], v[36:37], v[44:45]
	v_pk_mul_f32 v[46:47], v[38:39], v[46:47]
	v_cvt_pk_fp8_f32 v20, v40, v41
	v_cvt_pk_fp8_f32 v21, v44, v45
	v_cvt_pk_fp8_f32 v20, v42, v43 op_sel:[0,0,1]
	v_cvt_pk_fp8_f32 v21, v46, v47 op_sel:[0,0,1]
	v_pk_fma_f32 v[24:25], v[140:141], s[98:99], v[12:13] op_sel_hi:[1,0,1]
	v_pk_fma_f32 v[26:27], v[142:143], s[98:99], v[14:15] op_sel_hi:[1,0,1]
	v_pk_fma_f32 v[28:29], v[136:137], s[98:99], v[4:5] op_sel_hi:[1,0,1]
	v_pk_fma_f32 v[30:31], v[138:139], s[98:99], v[6:7] op_sel_hi:[1,0,1]
	v_pk_fma_f32 v[40:41], v[132:133], s[98:99], v[8:9] op_sel_hi:[1,0,1]
	v_pk_fma_f32 v[42:43], v[134:135], s[98:99], v[10:11] op_sel_hi:[1,0,1]
	v_pk_fma_f32 v[44:45], v[128:129], s[98:99], v[0:1] op_sel_hi:[1,0,1]
	v_pk_fma_f32 v[46:47], v[130:131], s[98:99], v[2:3] op_sel_hi:[1,0,1]
	v_min_f32_e32 v24, 0x40e00000, v24
	v_min_f32_e32 v25, 0x40e00000, v25
	v_min_f32_e32 v26, 0x40e00000, v26
	v_min_f32_e32 v27, 0x40e00000, v27
	v_min_f32_e32 v28, 0x40e00000, v28
	v_min_f32_e32 v29, 0x40e00000, v29
	v_min_f32_e32 v30, 0x40e00000, v30
; __device__ __forceinline__ unsigned pk4_fp8(float a, float b, float c, float d) { int w = __builtin_amdgcn_cvt_pk_fp8_f32(a, b, 0, false); w = __builtin_amdgcn_cvt_pk_fp8_f32(c, d, w, true); return (unsigned)w; }
;     __device__ __forceinline__ void operator()(const f32x4 (&acc)[2][2][4][2], const Unit& u, int wr, int wc, int fr, int fq) const {
;     ...
;                 for (int mi = 0; mi < 2; ++mi) { const int m = 2 * mp + mi;
;                     const f32x4 g0 = acc[ai][0][m][0] * ascale + bg0, g1 = acc[ai][0][m][1] * ascale + bg1, u0 = acc[ai][1][m][0] * ascale + bu0, u1 = acc[ai][1][m][1] * ascale + bu1;
;                     float r[8];
; #pragma unroll
;                     for (int j = 0; j < 4; ++j) {
;                         float gg = fminf(g0[j], 7.f), uu = fminf(fmaxf(u0[j], -7.f), 7.f); r[j] = 4.f * (uu + 1.f) * gg * __builtin_amdgcn_rcpf(1.f + __expf(-1.702f * gg));
;                         gg = fminf(g1[j], 7.f); uu = fminf(fmaxf(u1[j], -7.f), 7.f); r[4 + j] = 4.f * (uu + 1.f) * gg * __builtin_amdgcn_rcpf(1.f + __expf(-1.702f * gg));
;                     }
;                     wq[mi].x = pk4_fp8(r[0], r[1], r[2], r[3]); wq[mi].y = pk4_fp8(r[4], r[5], r[6], r[7]); }
;                 *(u32x4*)(act + (size_t)(row0 + ai * HALF + (2 * mp + (fq & 1)) * 16) * EFF + (c0 - 8 * (fq & 1))) = widen16(wq[0], wq[1]);
	v_min_f32_e32 v31, 0x40e00000, v31
	v_med3_f32 v40, v40, s74, v203
	v_med3_f32 v41, v41, s74, v203
	v_med3_f32 v42, v42, s74, v203
	v_med3_f32 v43, v43, s74, v203
	v_med3_f32 v44, v44, s74, v203
	v_med3_f32 v45, v45, s74, v203
	v_med3_f32 v46, v46, s74, v203
	v_med3_f32 v47, v47, s74, v203
	v_pk_mul_f32 v[32:33], v[24:25], s[98:99] op_sel:[0,1] op_sel_hi:[1,1]
	v_pk_mul_f32 v[34:35], v[26:27], s[98:99] op_sel:[0,1] op_sel_hi:[1,1]
	v_pk_mul_f32 v[36:37], v[28:29], s[98:99] op_sel:[0,1] op_sel_hi:[1,1]
	v_pk_mul_f32 v[38:39], v[30:31], s[98:99] op_sel:[0,1] op_sel_hi:[1,1]
	v_pk_mul_f32 v[32:33], v[32:33], s[100:101] op_sel_hi:[1,0]
	v_pk_mul_f32 v[34:35], v[34:35], s[100:101] op_sel_hi:[1,0]
	v_pk_mul_f32 v[36:37], v[36:37], s[100:101] op_sel_hi:[1,0]
	v_pk_mul_f32 v[38:39], v[38:39], s[100:101] op_sel_hi:[1,0]
	v_pk_fma_f32 v[40:41], v[40:41], 4.0, 4.0 op_sel_hi:[1,0,0]
	v_pk_fma_f32 v[42:43], v[42:43], 4.0, 4.0 op_sel_hi:[1,0,0]
	v_pk_fma_f32 v[44:45], v[44:45], 4.0, 4.0 op_sel_hi:[1,0,0]
	v_pk_fma_f32 v[46:47], v[46:47], 4.0, 4.0 op_sel_hi:[1,0,0]
	v_exp_f32_e32 v32, v32
	v_exp_f32_e32 v33, v33
	v_exp_f32_e32 v34, v34
	v_exp_f32_e32 v35, v35
	v_exp_f32_e32 v36, v36
	v_exp_f32_e32 v37, v37
	v_exp_f32_e32 v38, v38
	v_exp_f32_e32 v39, v39
	v_pk_mul_f32 v[40:41], v[24:25], v[40:41]
	v_pk_mul_f32 v[42:43], v[26:27], v[42:43]
	v_pk_mul_f32 v[44:45], v[28:29], v[44:45]
	v_pk_mul_f32 v[46:47], v[30:31], v[46:47]
	v_pk_add_f32 v[32:33], v[32:33], 1.0 op_sel_hi:[1,0]
	v_pk_add_f32 v[34:35], v[34:35], 1.0 op_sel_hi:[1,0]
	v_pk_add_f32 v[36:37], v[36:37], 1.0 op_sel_hi:[1,0]
	v_pk_add_f32 v[38:39], v[38:39], 1.0 op_sel_hi:[1,0]
	v_rcp_f32_e32 v32, v32
	v_rcp_f32_e32 v33, v33
	v_rcp_f32_e32 v34, v34
	v_rcp_f32_e32 v35, v35
	v_rcp_f32_e32 v36, v36
	v_rcp_f32_e32 v37, v37
	v_rcp_f32_e32 v38, v38
	v_rcp_f32_e32 v39, v39
	v_pk_mul_f32 v[40:41], v[32:33], v[40:41]
	v_pk_mul_f32 v[42:43], v[34:35], v[42:43]
	v_pk_mul_f32 v[44:45], v[36:37], v[44:45]
	v_pk_mul_f32 v[46:47], v[38:39], v[46:47]
	v_cvt_pk_fp8_f32 v22, v40, v41
	v_cvt_pk_fp8_f32 v23, v44, v45
	v_cvt_pk_fp8_f32 v22, v42, v43 op_sel:[0,0,1]
	v_cvt_pk_fp8_f32 v23, v46, v47 op_sel:[0,0,1]
	v_lshl_add_u64 v[50:51], v[48:49], 0, v[52:53]
	s_nop 1
	v_permlane16_swap_b32_e32 v20, v22
	v_permlane16_swap_b32_e32 v21, v23
	global_store_dwordx4 v[50:51], v[20:23], off
	v_pk_fma_f32 v[24:25], v[124:125], s[98:99], v[12:13] op_sel_hi:[1,0,1]
	v_pk_fma_f32 v[26:27], v[126:127], s[98:99], v[14:15] op_sel_hi:[1,0,1]
	v_pk_fma_f32 v[28:29], v[120:121], s[98:99], v[4:5] op_sel_hi:[1,0,1]
	v_pk_fma_f32 v[30:31], v[122:123], s[98:99], v[6:7] op_sel_hi:[1,0,1]
	v_pk_fma_f32 v[40:41], v[116:117], s[98:99], v[8:9] op_sel_hi:[1,0,1]
	v_pk_fma_f32 v[42:43], v[118:119], s[98:99], v[10:11] op_sel_hi:[1,0,1]
	v_pk_fma_f32 v[44:45], v[112:113], s[98:99], v[0:1] op_sel_hi:[1,0,1]
	v_pk_fma_f32 v[46:47], v[114:115], s[98:99], v[2:3] op_sel_hi:[1,0,1]
	v_min_f32_e32 v24, 0x40e00000, v24
	v_min_f32_e32 v25, 0x40e00000, v25
	v_min_f32_e32 v26, 0x40e00000, v26
	v_min_f32_e32 v27, 0x40e00000, v27
	v_min_f32_e32 v28, 0x40e00000, v28
	v_min_f32_e32 v29, 0x40e00000, v29
	v_min_f32_e32 v30, 0x40e00000, v30
	v_min_f32_e32 v31, 0x40e00000, v31
	v_med3_f32 v40, v40, s74, v203
	v_med3_f32 v41, v41, s74, v203
	v_med3_f32 v42, v42, s74, v203
	v_med3_f32 v43, v43, s74, v203
	v_med3_f32 v44, v44, s74, v203
	v_med3_f32 v45, v45, s74, v203
	v_med3_f32 v46, v46, s74, v203
	v_med3_f32 v47, v47, s74, v203
	v_pk_mul_f32 v[32:33], v[24:25], s[98:99] op_sel:[0,1] op_sel_hi:[1,1]
	v_pk_mul_f32 v[34:35], v[26:27], s[98:99] op_sel:[0,1] op_sel_hi:[1,1]
	v_pk_mul_f32 v[36:37], v[28:29], s[98:99] op_sel:[0,1] op_sel_hi:[1,1]
	v_pk_mul_f32 v[38:39], v[30:31], s[98:99] op_sel:[0,1] op_sel_hi:[1,1]
	v_pk_mul_f32 v[32:33], v[32:33], s[100:101] op_sel_hi:[1,0]
	v_pk_mul_f32 v[34:35], v[34:35], s[100:101] op_sel_hi:[1,0]
	v_pk_mul_f32 v[36:37], v[36:37], s[100:101] op_sel_hi:[1,0]
	v_pk_mul_f32 v[38:39], v[38:39], s[100:101] op_sel_hi:[1,0]
	v_pk_fma_f32 v[40:41], v[40:41], 4.0, 4.0 op_sel_hi:[1,0,0]
	v_pk_fma_f32 v[42:43], v[42:43], 4.0, 4.0 op_sel_hi:[1,0,0]
	v_pk_fma_f32 v[44:45], v[44:45], 4.0, 4.0 op_sel_hi:[1,0,0]
	v_pk_fma_f32 v[46:47], v[46:47], 4.0, 4.0 op_sel_hi:[1,0,0]
	v_exp_f32_e32 v32, v32
	v_exp_f32_e32 v33, v33
	v_exp_f32_e32 v34, v34
	v_exp_f32_e32 v35, v35
	v_exp_f32_e32 v36, v36
	v_exp_f32_e32 v37, v37
	v_exp_f32_e32 v38, v38
	v_exp_f32_e32 v39, v39
	v_pk_mul_f32 v[40:41], v[24:25], v[40:41]
	v_pk_mul_f32 v[42:43], v[26:27], v[42:43]
	v_pk_mul_f32 v[44:45], v[28:29], v[44:45]
	v_pk_mul_f32 v[46:47], v[30:31], v[46:47]
	v_pk_add_f32 v[32:33], v[32:33], 1.0 op_sel_hi:[1,0]
	v_pk_add_f32 v[34:35], v[34:35], 1.0 op_sel_hi:[1,0]
	v_pk_add_f32 v[36:37], v[36:37], 1.0 op_sel_hi:[1,0]
	v_pk_add_f32 v[38:39], v[38:39], 1.0 op_sel_hi:[1,0]
	v_rcp_f32_e32 v32, v32
	v_rcp_f32_e32 v33, v33
	v_rcp_f32_e32 v34, v34
	v_rcp_f32_e32 v35, v35
	v_rcp_f32_e32 v36, v36
	v_rcp_f32_e32 v37, v37
	v_rcp_f32_e32 v38, v38
	v_rcp_f32_e32 v39, v39
	v_pk_mul_f32 v[40:41], v[32:33], v[40:41]
	v_pk_mul_f32 v[42:43], v[34:35], v[42:43]
	v_pk_mul_f32 v[44:45], v[36:37], v[44:45]
	v_pk_mul_f32 v[46:47], v[38:39], v[46:47]
	v_cvt_pk_fp8_f32 v20, v40, v41
	v_cvt_pk_fp8_f32 v21, v44, v45
	v_cvt_pk_fp8_f32 v20, v42, v43 op_sel:[0,0,1]
	v_cvt_pk_fp8_f32 v21, v46, v47 op_sel:[0,0,1]
	v_pk_fma_f32 v[24:25], v[108:109], s[98:99], v[12:13] op_sel_hi:[1,0,1]
	v_pk_fma_f32 v[26:27], v[110:111], s[98:99], v[14:15] op_sel_hi:[1,0,1]
	v_pk_fma_f32 v[28:29], v[104:105], s[98:99], v[4:5] op_sel_hi:[1,0,1]
	v_pk_fma_f32 v[30:31], v[106:107], s[98:99], v[6:7] op_sel_hi:[1,0,1]
; __device__ __forceinline__ unsigned pk4_fp8(float a, float b, float c, float d) { int w = __builtin_amdgcn_cvt_pk_fp8_f32(a, b, 0, false); w = __builtin_amdgcn_cvt_pk_fp8_f32(c, d, w, true); return (unsigned)w; }
;     __device__ __forceinline__ void operator()(const f32x4 (&acc)[2][2][4][2], const Unit& u, int wr, int wc, int fr, int fq) const {
;     ...
;                 for (int mi = 0; mi < 2; ++mi) { const int m = 2 * mp + mi;
;                     const f32x4 g0 = acc[ai][0][m][0] * ascale + bg0, g1 = acc[ai][0][m][1] * ascale + bg1, u0 = acc[ai][1][m][0] * ascale + bu0, u1 = acc[ai][1][m][1] * ascale + bu1;
;                     float r[8];
; #pragma unroll
;                     for (int j = 0; j < 4; ++j) {
;                         float gg = fminf(g0[j], 7.f), uu = fminf(fmaxf(u0[j], -7.f), 7.f); r[j] = 4.f * (uu + 1.f) * gg * __builtin_amdgcn_rcpf(1.f + __expf(-1.702f * gg));
;                         gg = fminf(g1[j], 7.f); uu = fminf(fmaxf(u1[j], -7.f), 7.f); r[4 + j] = 4.f * (uu + 1.f) * gg * __builtin_amdgcn_rcpf(1.f + __expf(-1.702f * gg));
;                     }
;                     wq[mi].x = pk4_fp8(r[0], r[1], r[2], r[3]); wq[mi].y = pk4_fp8(r[4], r[5], r[6], r[7]); }
;                 *(u32x4*)(act + (size_t)(row0 + ai * HALF + (2 * mp + (fq & 1)) * 16) * EFF + (c0 - 8 * (fq & 1))) = widen16(wq[0], wq[1]);
	v_pk_fma_f32 v[40:41], v[100:101], s[98:99], v[8:9] op_sel_hi:[1,0,1]
	v_pk_fma_f32 v[42:43], v[102:103], s[98:99], v[10:11] op_sel_hi:[1,0,1]
	v_pk_fma_f32 v[44:45], v[96:97], s[98:99], v[0:1] op_sel_hi:[1,0,1]
	v_pk_fma_f32 v[46:47], v[98:99], s[98:99], v[2:3] op_sel_hi:[1,0,1]
	v_min_f32_e32 v24, 0x40e00000, v24
	v_min_f32_e32 v25, 0x40e00000, v25
	v_min_f32_e32 v26, 0x40e00000, v26
	v_min_f32_e32 v27, 0x40e00000, v27
	v_min_f32_e32 v28, 0x40e00000, v28
	v_min_f32_e32 v29, 0x40e00000, v29
	v_min_f32_e32 v30, 0x40e00000, v30
	v_min_f32_e32 v31, 0x40e00000, v31
	v_med3_f32 v40, v40, s74, v203
	v_med3_f32 v41, v41, s74, v203
	v_med3_f32 v42, v42, s74, v203
	v_med3_f32 v43, v43, s74, v203
	v_med3_f32 v44, v44, s74, v203
	v_med3_f32 v45, v45, s74, v203
	v_med3_f32 v46, v46, s74, v203
	v_med3_f32 v47, v47, s74, v203
	v_pk_mul_f32 v[32:33], v[24:25], s[98:99] op_sel:[0,1] op_sel_hi:[1,1]
	v_pk_mul_f32 v[34:35], v[26:27], s[98:99] op_sel:[0,1] op_sel_hi:[1,1]
	v_pk_mul_f32 v[36:37], v[28:29], s[98:99] op_sel:[0,1] op_sel_hi:[1,1]
	v_pk_mul_f32 v[38:39], v[30:31], s[98:99] op_sel:[0,1] op_sel_hi:[1,1]
	v_pk_mul_f32 v[32:33], v[32:33], s[100:101] op_sel_hi:[1,0]
	v_pk_mul_f32 v[34:35], v[34:35], s[100:101] op_sel_hi:[1,0]
	v_pk_mul_f32 v[36:37], v[36:37], s[100:101] op_sel_hi:[1,0]
	v_pk_mul_f32 v[38:39], v[38:39], s[100:101] op_sel_hi:[1,0]
	v_pk_fma_f32 v[40:41], v[40:41], 4.0, 4.0 op_sel_hi:[1,0,0]
	v_pk_fma_f32 v[42:43], v[42:43], 4.0, 4.0 op_sel_hi:[1,0,0]
	v_pk_fma_f32 v[44:45], v[44:45], 4.0, 4.0 op_sel_hi:[1,0,0]
	v_pk_fma_f32 v[46:47], v[46:47], 4.0, 4.0 op_sel_hi:[1,0,0]
	v_exp_f32_e32 v32, v32
	v_exp_f32_e32 v33, v33
	v_exp_f32_e32 v34, v34
	v_exp_f32_e32 v35, v35
	v_exp_f32_e32 v36, v36
	v_exp_f32_e32 v37, v37
	v_exp_f32_e32 v38, v38
	v_exp_f32_e32 v39, v39
	v_pk_mul_f32 v[40:41], v[24:25], v[40:41]
	v_pk_mul_f32 v[42:43], v[26:27], v[42:43]
	v_pk_mul_f32 v[44:45], v[28:29], v[44:45]
	v_pk_mul_f32 v[46:47], v[30:31], v[46:47]
	v_pk_add_f32 v[32:33], v[32:33], 1.0 op_sel_hi:[1,0]
	v_pk_add_f32 v[34:35], v[34:35], 1.0 op_sel_hi:[1,0]
	v_pk_add_f32 v[36:37], v[36:37], 1.0 op_sel_hi:[1,0]
	v_pk_add_f32 v[38:39], v[38:39], 1.0 op_sel_hi:[1,0]
	v_rcp_f32_e32 v32, v32
	v_rcp_f32_e32 v33, v33
	v_rcp_f32_e32 v34, v34
	v_rcp_f32_e32 v35, v35
	v_rcp_f32_e32 v36, v36
	v_rcp_f32_e32 v37, v37
	v_rcp_f32_e32 v38, v38
	v_rcp_f32_e32 v39, v39
	v_pk_mul_f32 v[40:41], v[32:33], v[40:41]
	v_pk_mul_f32 v[42:43], v[34:35], v[42:43]
	v_pk_mul_f32 v[44:45], v[36:37], v[44:45]
	v_pk_mul_f32 v[46:47], v[38:39], v[46:47]
	v_cvt_pk_fp8_f32 v22, v40, v41
	v_cvt_pk_fp8_f32 v23, v44, v45
	v_cvt_pk_fp8_f32 v22, v42, v43 op_sel:[0,0,1]
	v_cvt_pk_fp8_f32 v23, v46, v47 op_sel:[0,0,1]
	v_lshl_add_u64 v[50:51], v[48:49], 0, v[54:55]
	s_nop 1
	v_permlane16_swap_b32_e32 v20, v22
	v_permlane16_swap_b32_e32 v21, v23
	global_store_dwordx4 v[50:51], v[20:23], off
	v_pk_fma_f32 v[24:25], v[92:93], s[98:99], v[12:13] op_sel_hi:[1,0,1]
	v_pk_fma_f32 v[26:27], v[94:95], s[98:99], v[14:15] op_sel_hi:[1,0,1]
	v_pk_fma_f32 v[28:29], v[88:89], s[98:99], v[4:5] op_sel_hi:[1,0,1]
	v_pk_fma_f32 v[30:31], v[90:91], s[98:99], v[6:7] op_sel_hi:[1,0,1]
	v_pk_fma_f32 v[40:41], v[84:85], s[98:99], v[8:9] op_sel_hi:[1,0,1]
	v_pk_fma_f32 v[42:43], v[86:87], s[98:99], v[10:11] op_sel_hi:[1,0,1]
	v_pk_fma_f32 v[44:45], v[80:81], s[98:99], v[0:1] op_sel_hi:[1,0,1]
	v_pk_fma_f32 v[46:47], v[82:83], s[98:99], v[2:3] op_sel_hi:[1,0,1]
	v_min_f32_e32 v24, 0x40e00000, v24
	v_min_f32_e32 v25, 0x40e00000, v25
	v_min_f32_e32 v26, 0x40e00000, v26
	v_min_f32_e32 v27, 0x40e00000, v27
	v_min_f32_e32 v28, 0x40e00000, v28
	v_min_f32_e32 v29, 0x40e00000, v29
	v_min_f32_e32 v30, 0x40e00000, v30
	v_min_f32_e32 v31, 0x40e00000, v31
	v_med3_f32 v40, v40, s74, v203
	v_med3_f32 v41, v41, s74, v203
	v_med3_f32 v42, v42, s74, v203
	v_med3_f32 v43, v43, s74, v203
	v_med3_f32 v44, v44, s74, v203
	v_med3_f32 v45, v45, s74, v203
	v_med3_f32 v46, v46, s74, v203
	v_med3_f32 v47, v47, s74, v203
	v_pk_mul_f32 v[32:33], v[24:25], s[98:99] op_sel:[0,1] op_sel_hi:[1,1]
	v_pk_mul_f32 v[34:35], v[26:27], s[98:99] op_sel:[0,1] op_sel_hi:[1,1]
	v_pk_mul_f32 v[36:37], v[28:29], s[98:99] op_sel:[0,1] op_sel_hi:[1,1]
	v_pk_mul_f32 v[38:39], v[30:31], s[98:99] op_sel:[0,1] op_sel_hi:[1,1]
	v_pk_mul_f32 v[32:33], v[32:33], s[100:101] op_sel_hi:[1,0]
	v_pk_mul_f32 v[34:35], v[34:35], s[100:101] op_sel_hi:[1,0]
	v_pk_mul_f32 v[36:37], v[36:37], s[100:101] op_sel_hi:[1,0]
	v_pk_mul_f32 v[38:39], v[38:39], s[100:101] op_sel_hi:[1,0]
	v_pk_fma_f32 v[40:41], v[40:41], 4.0, 4.0 op_sel_hi:[1,0,0]
; #define PG8_BAR __builtin_amdgcn_s_barrier()
; __device__ __forceinline__ unsigned pk4_fp8(float a, float b, float c, float d) { int w = __builtin_amdgcn_cvt_pk_fp8_f32(a, b, 0, false); w = __builtin_amdgcn_cvt_pk_fp8_f32(c, d, w, true); return (unsigned)w; }
; template <class Epi, class Sched, bool ALIGN_EPI = true, bool SP2 = true, bool FP8 = false, bool GATHER = false>
; __device__ __forceinline__ void gemm_phase(LAS unsigned char* lds, const Dims g, const Sched& S, const Epi& E, const int wv) {
;     ...
;         if (!has_next) break;
; #pragma unroll
;         for (int a = 0; a < 2; ++a)
; #pragma unroll
;             for (int b = 0; b < 2; ++b)
; #pragma unroll
;                 for (int m = 0; m < 4; ++m)
; #pragma unroll
;                     for (int n = 0; n < 2; ++n) acc[a][b][m][n] = (f32x4){0.f, 0.f, 0.f, 0.f};
;         cur = nxt; cA = nA; cB = nB; ++ui;
;         if constexpr (ALIGN_EPI) { if (wr == 1) PG8_BAR; }
;     __device__ __forceinline__ void operator()(const f32x4 (&acc)[2][2][4][2], const Unit& u, int wr, int wc, int fr, int fq) const {
;     ...
;                 for (int mi = 0; mi < 2; ++mi) { const int m = 2 * mp + mi;
;                     const f32x4 g0 = acc[ai][0][m][0] * ascale + bg0, g1 = acc[ai][0][m][1] * ascale + bg1, u0 = acc[ai][1][m][0] * ascale + bu0, u1 = acc[ai][1][m][1] * ascale + bu1;
;                     float r[8];
; #pragma unroll
;                     for (int j = 0; j < 4; ++j) {
;                         float gg = fminf(g0[j], 7.f), uu = fminf(fmaxf(u0[j], -7.f), 7.f); r[j] = 4.f * (uu + 1.f) * gg * __builtin_amdgcn_rcpf(1.f + __expf(-1.702f * gg));
;                         gg = fminf(g1[j], 7.f); uu = fminf(fmaxf(u1[j], -7.f), 7.f); r[4 + j] = 4.f * (uu + 1.f) * gg * __builtin_amdgcn_rcpf(1.f + __expf(-1.702f * gg));
;                     }
;                     wq[mi].x = pk4_fp8(r[0], r[1], r[2], r[3]); wq[mi].y = pk4_fp8(r[4], r[5], r[6], r[7]); }
;                 *(u32x4*)(act + (size_t)(row0 + ai * HALF + (2 * mp + (fq & 1)) * 16) * EFF + (c0 - 8 * (fq & 1))) = widen16(wq[0], wq[1]);
;             }
	v_pk_fma_f32 v[42:43], v[42:43], 4.0, 4.0 op_sel_hi:[1,0,0]
	v_pk_fma_f32 v[44:45], v[44:45], 4.0, 4.0 op_sel_hi:[1,0,0]
	v_pk_fma_f32 v[46:47], v[46:47], 4.0, 4.0 op_sel_hi:[1,0,0]
	v_exp_f32_e32 v32, v32
	v_exp_f32_e32 v33, v33
	v_exp_f32_e32 v34, v34
	v_exp_f32_e32 v35, v35
	v_exp_f32_e32 v36, v36
	v_exp_f32_e32 v37, v37
	v_exp_f32_e32 v38, v38
	v_exp_f32_e32 v39, v39
	v_pk_mul_f32 v[40:41], v[24:25], v[40:41]
	v_pk_mul_f32 v[42:43], v[26:27], v[42:43]
	v_pk_mul_f32 v[44:45], v[28:29], v[44:45]
	v_pk_mul_f32 v[46:47], v[30:31], v[46:47]
	v_pk_add_f32 v[32:33], v[32:33], 1.0 op_sel_hi:[1,0]
	v_pk_add_f32 v[34:35], v[34:35], 1.0 op_sel_hi:[1,0]
	v_pk_add_f32 v[36:37], v[36:37], 1.0 op_sel_hi:[1,0]
	v_pk_add_f32 v[38:39], v[38:39], 1.0 op_sel_hi:[1,0]
	v_rcp_f32_e32 v32, v32
	v_rcp_f32_e32 v33, v33
	v_rcp_f32_e32 v34, v34
	v_rcp_f32_e32 v35, v35
	v_rcp_f32_e32 v36, v36
	v_rcp_f32_e32 v37, v37
	v_rcp_f32_e32 v38, v38
	v_rcp_f32_e32 v39, v39
	v_pk_mul_f32 v[40:41], v[32:33], v[40:41]
	v_pk_mul_f32 v[42:43], v[34:35], v[42:43]
	v_pk_mul_f32 v[44:45], v[36:37], v[44:45]
	v_pk_mul_f32 v[46:47], v[38:39], v[46:47]
	v_cvt_pk_fp8_f32 v20, v40, v41
	v_cvt_pk_fp8_f32 v21, v44, v45
	v_cvt_pk_fp8_f32 v20, v42, v43 op_sel:[0,0,1]
	v_cvt_pk_fp8_f32 v21, v46, v47 op_sel:[0,0,1]
	v_pk_fma_f32 v[24:25], v[76:77], s[98:99], v[12:13] op_sel_hi:[1,0,1]
	v_pk_fma_f32 v[26:27], v[78:79], s[98:99], v[14:15] op_sel_hi:[1,0,1]
	v_pk_fma_f32 v[28:29], v[72:73], s[98:99], v[4:5] op_sel_hi:[1,0,1]
	v_pk_fma_f32 v[30:31], v[74:75], s[98:99], v[6:7] op_sel_hi:[1,0,1]
	v_pk_fma_f32 v[40:41], v[68:69], s[98:99], v[8:9] op_sel_hi:[1,0,1]
	v_pk_fma_f32 v[42:43], v[70:71], s[98:99], v[10:11] op_sel_hi:[1,0,1]
	v_pk_fma_f32 v[44:45], v[64:65], s[98:99], v[0:1] op_sel_hi:[1,0,1]
	v_pk_fma_f32 v[46:47], v[66:67], s[98:99], v[2:3] op_sel_hi:[1,0,1]
	v_min_f32_e32 v24, 0x40e00000, v24
	v_min_f32_e32 v25, 0x40e00000, v25
	v_min_f32_e32 v26, 0x40e00000, v26
	v_min_f32_e32 v27, 0x40e00000, v27
	v_min_f32_e32 v28, 0x40e00000, v28
	v_min_f32_e32 v29, 0x40e00000, v29
	v_min_f32_e32 v30, 0x40e00000, v30
	v_min_f32_e32 v31, 0x40e00000, v31
	v_med3_f32 v40, v40, s74, v203
	v_med3_f32 v41, v41, s74, v203
	v_med3_f32 v42, v42, s74, v203
	v_med3_f32 v43, v43, s74, v203
	v_med3_f32 v44, v44, s74, v203
	v_med3_f32 v45, v45, s74, v203
	v_med3_f32 v46, v46, s74, v203
	v_med3_f32 v47, v47, s74, v203
	v_pk_mul_f32 v[32:33], v[24:25], s[98:99] op_sel:[0,1] op_sel_hi:[1,1]
	v_pk_mul_f32 v[34:35], v[26:27], s[98:99] op_sel:[0,1] op_sel_hi:[1,1]
	v_pk_mul_f32 v[36:37], v[28:29], s[98:99] op_sel:[0,1] op_sel_hi:[1,1]
	v_pk_mul_f32 v[38:39], v[30:31], s[98:99] op_sel:[0,1] op_sel_hi:[1,1]
	v_pk_mul_f32 v[32:33], v[32:33], s[100:101] op_sel_hi:[1,0]
	v_pk_mul_f32 v[34:35], v[34:35], s[100:101] op_sel_hi:[1,0]
	v_pk_mul_f32 v[36:37], v[36:37], s[100:101] op_sel_hi:[1,0]
	v_pk_mul_f32 v[38:39], v[38:39], s[100:101] op_sel_hi:[1,0]
	v_pk_fma_f32 v[40:41], v[40:41], 4.0, 4.0 op_sel_hi:[1,0,0]
	v_pk_fma_f32 v[42:43], v[42:43], 4.0, 4.0 op_sel_hi:[1,0,0]
	v_pk_fma_f32 v[44:45], v[44:45], 4.0, 4.0 op_sel_hi:[1,0,0]
	v_pk_fma_f32 v[46:47], v[46:47], 4.0, 4.0 op_sel_hi:[1,0,0]
	v_exp_f32_e32 v32, v32
	v_exp_f32_e32 v33, v33
	v_exp_f32_e32 v34, v34
	v_exp_f32_e32 v35, v35
	v_exp_f32_e32 v36, v36
	v_exp_f32_e32 v37, v37
	v_exp_f32_e32 v38, v38
	v_exp_f32_e32 v39, v39
	v_pk_mul_f32 v[40:41], v[24:25], v[40:41]
	v_pk_mul_f32 v[42:43], v[26:27], v[42:43]
	v_pk_mul_f32 v[44:45], v[28:29], v[44:45]
	v_pk_mul_f32 v[46:47], v[30:31], v[46:47]
	v_pk_add_f32 v[32:33], v[32:33], 1.0 op_sel_hi:[1,0]
	v_pk_add_f32 v[34:35], v[34:35], 1.0 op_sel_hi:[1,0]
	v_pk_add_f32 v[36:37], v[36:37], 1.0 op_sel_hi:[1,0]
	v_pk_add_f32 v[38:39], v[38:39], 1.0 op_sel_hi:[1,0]
	v_rcp_f32_e32 v32, v32
	v_rcp_f32_e32 v33, v33
	v_rcp_f32_e32 v34, v34
	v_rcp_f32_e32 v35, v35
	v_rcp_f32_e32 v36, v36
	v_rcp_f32_e32 v37, v37
	v_rcp_f32_e32 v38, v38
	v_rcp_f32_e32 v39, v39
	v_pk_mul_f32 v[40:41], v[32:33], v[40:41]
	v_pk_mul_f32 v[42:43], v[34:35], v[42:43]
	v_pk_mul_f32 v[44:45], v[36:37], v[44:45]
	v_pk_mul_f32 v[46:47], v[38:39], v[46:47]
	v_cvt_pk_fp8_f32 v22, v40, v41
	v_cvt_pk_fp8_f32 v23, v44, v45
	v_cvt_pk_fp8_f32 v22, v42, v43 op_sel:[0,0,1]
	v_cvt_pk_fp8_f32 v23, v46, v47 op_sel:[0,0,1]
	v_lshl_add_u64 v[50:51], v[48:49], 0, v[54:55]
	v_lshl_add_u64 v[50:51], v[50:51], 0, v[52:53]
	s_nop 1
	v_permlane16_swap_b32_e32 v20, v22
	v_permlane16_swap_b32_e32 v21, v23
	global_store_dwordx4 v[50:51], v[20:23], off
	s_cbranch_vccnz .LBB0_1419
	s_andn2_b64 vcc, exec, s[14:15]
	s_cbranch_vccnz .LBB0_1418
	s_barrier
	s_branch .LBB0_1418

; __device__ __forceinline__ unsigned pk4_fp8(float a, float b, float c, float d) { int w = __builtin_amdgcn_cvt_pk_fp8_f32(a, b, 0, false); w = __builtin_amdgcn_cvt_pk_fp8_f32(c, d, w, true); return (unsigned)w; }
;     __device__ __forceinline__ void operator()(const f32x4 (&acc)[2][2][4][2], const Unit& u, int wr, int wc, int fr, int fq) const {
;         const int row0 = u.pm * BM + wr * 64 + fr, c0 = u.pn * HALF + wc * 32 + 8 * fq;
;         const float* bp = bgu + (size_t)u.aux * 2048 + c0;
;         const f32x4 bg0 = *(const f32x4*)(bp), bg1 = *(const f32x4*)(bp + 4), bu0 = *(const f32x4*)(bp + 1024), bu1 = *(const f32x4*)(bp + 1028);
; #pragma unroll
;         for (int ai = 0; ai < 2; ++ai)
; #pragma unroll
;             for (int mp = 0; mp < 2; ++mp) {
;                 u32x2 wq[2];
; #pragma unroll
;                 for (int mi = 0; mi < 2; ++mi) { const int m = 2 * mp + mi;
;                     const f32x4 g0 = acc[ai][0][m][0] * ascale + bg0, g1 = acc[ai][0][m][1] * ascale + bg1, u0 = acc[ai][1][m][0] * ascale + bu0, u1 = acc[ai][1][m][1] * ascale + bu1;
;                     float r[8];
; #pragma unroll
;                     for (int j = 0; j < 4; ++j) {
;                         float gg = fminf(g0[j], 7.f), uu = fminf(fmaxf(u0[j], -7.f), 7.f); r[j] = 4.f * (uu + 1.f) * gg * __builtin_amdgcn_rcpf(1.f + __expf(-1.702f * gg));
;                         gg = fminf(g1[j], 7.f); uu = fminf(fmaxf(u1[j], -7.f), 7.f); r[4 + j] = 4.f * (uu + 1.f) * gg * __builtin_amdgcn_rcpf(1.f + __expf(-1.702f * gg));
;                     }
;                     wq[mi].x = pk4_fp8(r[0], r[1], r[2], r[3]); wq[mi].y = pk4_fp8(r[4], r[5], r[6], r[7]); }
;                 *(u32x4*)(act + (size_t)(row0 + ai * HALF + (2 * mp + (fq & 1)) * 16) * EFF + (c0 - 8 * (fq & 1))) = widen16(wq[0], wq[1]);
.LBB0_2537:
	v_mov_b32_e32 v18, v192
	s_lshl_b32 s26, s26, 7
	v_lshrrev_b32_e32 v0, 1, v18
	s_ashr_i32 s37, s36, 31
	s_lshl_b32 s38, s77, 8
	v_and_or_b32 v0, v0, 24, s26
	s_lshl_b64 s[36:37], s[36:37], 13
	v_or_b32_e32 v16, s64, v0
	s_add_u32 s36, s61, s36
	s_addc_u32 s37, s62, s37
	v_ashrrev_i32_e32 v17, 31, v16
	v_lshl_add_u64 v[0:1], v[16:17], 2, s[36:37]
	global_load_dwordx4 v[12:15], v[0:1], off
	global_load_dwordx4 v[4:7], v[0:1], off offset:16
	v_add_co_u32_e32 v2, vcc, s73, v0
	v_bfe_u32 v17, v18, 4, 1
	s_nop 0
	v_addc_co_u32_e32 v3, vcc, 0, v1, vcc
	v_lshl_add_u64 v[0:1], v[0:1], 0, s[16:17]
	global_load_dwordx4 v[8:11], v[2:3], off
	v_lshlrev_b32_e32 v19, 3, v17
	global_load_dwordx4 v[0:3], v[0:1], off offset:16
	v_sub_u32_e32 v16, v16, v19
	s_add_i32 s38, s38, s63
	v_and_or_b32 v18, v18, 15, s38
	v_lshl_or_b32 v18, v17, 4, v18
	v_ashrrev_i32_e32 v17, 31, v16
	s_andn2_b64 vcc, exec, s[24:25]
	s_mov_b64 s[24:25], -1
	s_waitcnt vmcnt(0)
	s_mov_b32 s98, 0x3a000000
	s_mov_b32 s99, 0xbfd9db23
	s_mov_b32 s100, 0x3fb8aa3b
	s_mov_b32 s101, 0
	v_ashrrev_i32_e32 v19, 31, v18
	v_lshlrev_b64 v[48:49], 10, v[18:19]
	v_lshl_add_u64 v[48:49], s[12:13], 0, v[48:49]
	v_lshl_add_u64 v[48:49], v[48:49], 0, v[16:17]
	v_mov_b32_e32 v52, 0x8000
	v_mov_b32_e32 v53, 0
	v_mov_b32_e32 v54, 0x20000
	v_mov_b32_e32 v55, 0
	v_pk_fma_f32 v[24:25], v[188:189], s[98:99], v[12:13] op_sel_hi:[1,0,1]
	v_pk_fma_f32 v[26:27], v[190:191], s[98:99], v[14:15] op_sel_hi:[1,0,1]
	v_pk_fma_f32 v[28:29], v[184:185], s[98:99], v[4:5] op_sel_hi:[1,0,1]
	v_pk_fma_f32 v[30:31], v[186:187], s[98:99], v[6:7] op_sel_hi:[1,0,1]
	v_pk_fma_f32 v[40:41], v[180:181], s[98:99], v[8:9] op_sel_hi:[1,0,1]
	v_pk_fma_f32 v[42:43], v[182:183], s[98:99], v[10:11] op_sel_hi:[1,0,1]
	v_pk_fma_f32 v[44:45], v[176:177], s[98:99], v[0:1] op_sel_hi:[1,0,1]
	v_pk_fma_f32 v[46:47], v[178:179], s[98:99], v[2:3] op_sel_hi:[1,0,1]
	v_min_f32_e32 v24, 0x40e00000, v24
	v_min_f32_e32 v25, 0x40e00000, v25
	v_min_f32_e32 v26, 0x40e00000, v26
	v_min_f32_e32 v27, 0x40e00000, v27
	v_min_f32_e32 v28, 0x40e00000, v28
	v_min_f32_e32 v29, 0x40e00000, v29
	v_min_f32_e32 v30, 0x40e00000, v30
	v_min_f32_e32 v31, 0x40e00000, v31
	v_med3_f32 v40, v40, s74, v203
	v_med3_f32 v41, v41, s74, v203
	v_med3_f32 v42, v42, s74, v203
	v_med3_f32 v43, v43, s74, v203
	v_med3_f32 v44, v44, s74, v203
	v_med3_f32 v45, v45, s74, v203
	v_med3_f32 v46, v46, s74, v203
	v_med3_f32 v47, v47, s74, v203
	v_pk_mul_f32 v[32:33], v[24:25], s[98:99] op_sel:[0,1] op_sel_hi:[1,1]
	v_pk_mul_f32 v[34:35], v[26:27], s[98:99] op_sel:[0,1] op_sel_hi:[1,1]
	v_pk_mul_f32 v[36:37], v[28:29], s[98:99] op_sel:[0,1] op_sel_hi:[1,1]
	v_pk_mul_f32 v[38:39], v[30:31], s[98:99] op_sel:[0,1] op_sel_hi:[1,1]
	v_pk_mul_f32 v[32:33], v[32:33], s[100:101] op_sel_hi:[1,0]
	v_pk_mul_f32 v[34:35], v[34:35], s[100:101] op_sel_hi:[1,0]
	v_pk_mul_f32 v[36:37], v[36:37], s[100:101] op_sel_hi:[1,0]
	v_pk_mul_f32 v[38:39], v[38:39], s[100:101] op_sel_hi:[1,0]
	v_pk_fma_f32 v[40:41], v[40:41], 4.0, 4.0 op_sel_hi:[1,0,0]
	v_pk_fma_f32 v[42:43], v[42:43], 4.0, 4.0 op_sel_hi:[1,0,0]
	v_pk_fma_f32 v[44:45], v[44:45], 4.0, 4.0 op_sel_hi:[1,0,0]
	v_pk_fma_f32 v[46:47], v[46:47], 4.0, 4.0 op_sel_hi:[1,0,0]
	v_exp_f32_e32 v32, v32
	v_exp_f32_e32 v33, v33
	v_exp_f32_e32 v34, v34
	v_exp_f32_e32 v35, v35
	v_exp_f32_e32 v36, v36
	v_exp_f32_e32 v37, v37
	v_exp_f32_e32 v38, v38
	v_exp_f32_e32 v39, v39
	v_pk_mul_f32 v[40:41], v[24:25], v[40:41]
	v_pk_mul_f32 v[42:43], v[26:27], v[42:43]
	v_pk_mul_f32 v[44:45], v[28:29], v[44:45]
	v_pk_mul_f32 v[46:47], v[30:31], v[46:47]
	v_pk_add_f32 v[32:33], v[32:33], 1.0 op_sel_hi:[1,0]
	v_pk_add_f32 v[34:35], v[34:35], 1.0 op_sel_hi:[1,0]
	v_pk_add_f32 v[36:37], v[36:37], 1.0 op_sel_hi:[1,0]
	v_pk_add_f32 v[38:39], v[38:39], 1.0 op_sel_hi:[1,0]
	v_rcp_f32_e32 v32, v32
	v_rcp_f32_e32 v33, v33
	v_rcp_f32_e32 v34, v34
	v_rcp_f32_e32 v35, v35
	v_rcp_f32_e32 v36, v36
	v_rcp_f32_e32 v37, v37
	v_rcp_f32_e32 v38, v38
	v_rcp_f32_e32 v39, v39
	v_pk_mul_f32 v[40:41], v[32:33], v[40:41]
	v_pk_mul_f32 v[42:43], v[34:35], v[42:43]
	v_pk_mul_f32 v[44:45], v[36:37], v[44:45]
	v_pk_mul_f32 v[46:47], v[38:39], v[46:47]
	v_cvt_pk_fp8_f32 v20, v40, v41
	v_cvt_pk_fp8_f32 v21, v44, v45
	v_cvt_pk_fp8_f32 v20, v42, v43 op_sel:[0,0,1]
	v_cvt_pk_fp8_f32 v21, v46, v47 op_sel:[0,0,1]
	v_pk_fma_f32 v[24:25], v[172:173], s[98:99], v[12:13] op_sel_hi:[1,0,1]
	v_pk_fma_f32 v[26:27], v[174:175], s[98:99], v[14:15] op_sel_hi:[1,0,1]
	v_pk_fma_f32 v[28:29], v[168:169], s[98:99], v[4:5] op_sel_hi:[1,0,1]
	v_pk_fma_f32 v[30:31], v[170:171], s[98:99], v[6:7] op_sel_hi:[1,0,1]
	v_pk_fma_f32 v[40:41], v[164:165], s[98:99], v[8:9] op_sel_hi:[1,0,1]
	v_pk_fma_f32 v[42:43], v[166:167], s[98:99], v[10:11] op_sel_hi:[1,0,1]
	v_pk_fma_f32 v[44:45], v[160:161], s[98:99], v[0:1] op_sel_hi:[1,0,1]
	v_pk_fma_f32 v[46:47], v[162:163], s[98:99], v[2:3] op_sel_hi:[1,0,1]
	v_min_f32_e32 v24, 0x40e00000, v24
	v_min_f32_e32 v25, 0x40e00000, v25
	v_min_f32_e32 v26, 0x40e00000, v26
	v_min_f32_e32 v27, 0x40e00000, v27
	v_min_f32_e32 v28, 0x40e00000, v28
	v_min_f32_e32 v29, 0x40e00000, v29
	v_min_f32_e32 v30, 0x40e00000, v30
	v_min_f32_e32 v31, 0x40e00000, v31
	v_med3_f32 v40, v40, s74, v203
	v_med3_f32 v41, v41, s74, v203
	v_med3_f32 v42, v42, s74, v203
	v_med3_f32 v43, v43, s74, v203
	v_med3_f32 v44, v44, s74, v203
	v_med3_f32 v45, v45, s74, v203
	v_med3_f32 v46, v46, s74, v203
	v_med3_f32 v47, v47, s74, v203
	v_pk_mul_f32 v[32:33], v[24:25], s[98:99] op_sel:[0,1] op_sel_hi:[1,1]
	v_pk_mul_f32 v[34:35], v[26:27], s[98:99] op_sel:[0,1] op_sel_hi:[1,1]
	v_pk_mul_f32 v[36:37], v[28:29], s[98:99] op_sel:[0,1] op_sel_hi:[1,1]
; __device__ __forceinline__ unsigned pk4_fp8(float a, float b, float c, float d) { int w = __builtin_amdgcn_cvt_pk_fp8_f32(a, b, 0, false); w = __builtin_amdgcn_cvt_pk_fp8_f32(c, d, w, true); return (unsigned)w; }
;     __device__ __forceinline__ void operator()(const f32x4 (&acc)[2][2][4][2], const Unit& u, int wr, int wc, int fr, int fq) const {
;     ...
;                 for (int mi = 0; mi < 2; ++mi) { const int m = 2 * mp + mi;
;                     const f32x4 g0 = acc[ai][0][m][0] * ascale + bg0, g1 = acc[ai][0][m][1] * ascale + bg1, u0 = acc[ai][1][m][0] * ascale + bu0, u1 = acc[ai][1][m][1] * ascale + bu1;
;                     float r[8];
; #pragma unroll
;                     for (int j = 0; j < 4; ++j) {
;                         float gg = fminf(g0[j], 7.f), uu = fminf(fmaxf(u0[j], -7.f), 7.f); r[j] = 4.f * (uu + 1.f) * gg * __builtin_amdgcn_rcpf(1.f + __expf(-1.702f * gg));
;                         gg = fminf(g1[j], 7.f); uu = fminf(fmaxf(u1[j], -7.f), 7.f); r[4 + j] = 4.f * (uu + 1.f) * gg * __builtin_amdgcn_rcpf(1.f + __expf(-1.702f * gg));
;                     }
;                     wq[mi].x = pk4_fp8(r[0], r[1], r[2], r[3]); wq[mi].y = pk4_fp8(r[4], r[5], r[6], r[7]); }
;                 *(u32x4*)(act + (size_t)(row0 + ai * HALF + (2 * mp + (fq & 1)) * 16) * EFF + (c0 - 8 * (fq & 1))) = widen16(wq[0], wq[1]);
	v_pk_mul_f32 v[38:39], v[30:31], s[98:99] op_sel:[0,1] op_sel_hi:[1,1]
	v_pk_mul_f32 v[32:33], v[32:33], s[100:101] op_sel_hi:[1,0]
	v_pk_mul_f32 v[34:35], v[34:35], s[100:101] op_sel_hi:[1,0]
	v_pk_mul_f32 v[36:37], v[36:37], s[100:101] op_sel_hi:[1,0]
	v_pk_mul_f32 v[38:39], v[38:39], s[100:101] op_sel_hi:[1,0]
	v_pk_fma_f32 v[40:41], v[40:41], 4.0, 4.0 op_sel_hi:[1,0,0]
	v_pk_fma_f32 v[42:43], v[42:43], 4.0, 4.0 op_sel_hi:[1,0,0]
	v_pk_fma_f32 v[44:45], v[44:45], 4.0, 4.0 op_sel_hi:[1,0,0]
	v_pk_fma_f32 v[46:47], v[46:47], 4.0, 4.0 op_sel_hi:[1,0,0]
	v_exp_f32_e32 v32, v32
	v_exp_f32_e32 v33, v33
	v_exp_f32_e32 v34, v34
	v_exp_f32_e32 v35, v35
	v_exp_f32_e32 v36, v36
	v_exp_f32_e32 v37, v37
	v_exp_f32_e32 v38, v38
	v_exp_f32_e32 v39, v39
	v_pk_mul_f32 v[40:41], v[24:25], v[40:41]
	v_pk_mul_f32 v[42:43], v[26:27], v[42:43]
	v_pk_mul_f32 v[44:45], v[28:29], v[44:45]
	v_pk_mul_f32 v[46:47], v[30:31], v[46:47]
	v_pk_add_f32 v[32:33], v[32:33], 1.0 op_sel_hi:[1,0]
	v_pk_add_f32 v[34:35], v[34:35], 1.0 op_sel_hi:[1,0]
	v_pk_add_f32 v[36:37], v[36:37], 1.0 op_sel_hi:[1,0]
	v_pk_add_f32 v[38:39], v[38:39], 1.0 op_sel_hi:[1,0]
	v_rcp_f32_e32 v32, v32
	v_rcp_f32_e32 v33, v33
	v_rcp_f32_e32 v34, v34
	v_rcp_f32_e32 v35, v35
	v_rcp_f32_e32 v36, v36
	v_rcp_f32_e32 v37, v37
	v_rcp_f32_e32 v38, v38
	v_rcp_f32_e32 v39, v39
	v_pk_mul_f32 v[40:41], v[32:33], v[40:41]
	v_pk_mul_f32 v[42:43], v[34:35], v[42:43]
	v_pk_mul_f32 v[44:45], v[36:37], v[44:45]
	v_pk_mul_f32 v[46:47], v[38:39], v[46:47]
	v_cvt_pk_fp8_f32 v22, v40, v41
	v_cvt_pk_fp8_f32 v23, v44, v45
	v_cvt_pk_fp8_f32 v22, v42, v43 op_sel:[0,0,1]
	v_cvt_pk_fp8_f32 v23, v46, v47 op_sel:[0,0,1]
	v_mov_b64_e32 v[50:51], v[48:49]
	s_nop 1
	v_permlane16_swap_b32_e32 v20, v22
	v_permlane16_swap_b32_e32 v21, v23
	global_store_dwordx4 v[50:51], v[20:23], off
	v_pk_fma_f32 v[24:25], v[156:157], s[98:99], v[12:13] op_sel_hi:[1,0,1]
	v_pk_fma_f32 v[26:27], v[158:159], s[98:99], v[14:15] op_sel_hi:[1,0,1]
	v_pk_fma_f32 v[28:29], v[152:153], s[98:99], v[4:5] op_sel_hi:[1,0,1]
	v_pk_fma_f32 v[30:31], v[154:155], s[98:99], v[6:7] op_sel_hi:[1,0,1]
	v_pk_fma_f32 v[40:41], v[148:149], s[98:99], v[8:9] op_sel_hi:[1,0,1]
	v_pk_fma_f32 v[42:43], v[150:151], s[98:99], v[10:11] op_sel_hi:[1,0,1]
	v_pk_fma_f32 v[44:45], v[144:145], s[98:99], v[0:1] op_sel_hi:[1,0,1]
	v_pk_fma_f32 v[46:47], v[146:147], s[98:99], v[2:3] op_sel_hi:[1,0,1]
	v_min_f32_e32 v24, 0x40e00000, v24
	v_min_f32_e32 v25, 0x40e00000, v25
	v_min_f32_e32 v26, 0x40e00000, v26
	v_min_f32_e32 v27, 0x40e00000, v27
	v_min_f32_e32 v28, 0x40e00000, v28
	v_min_f32_e32 v29, 0x40e00000, v29
	v_min_f32_e32 v30, 0x40e00000, v30
	v_min_f32_e32 v31, 0x40e00000, v31
	v_med3_f32 v40, v40, s74, v203
	v_med3_f32 v41, v41, s74, v203
	v_med3_f32 v42, v42, s74, v203
	v_med3_f32 v43, v43, s74, v203
	v_med3_f32 v44, v44, s74, v203
	v_med3_f32 v45, v45, s74, v203
	v_med3_f32 v46, v46, s74, v203
	v_med3_f32 v47, v47, s74, v203
	v_pk_mul_f32 v[32:33], v[24:25], s[98:99] op_sel:[0,1] op_sel_hi:[1,1]
	v_pk_mul_f32 v[34:35], v[26:27], s[98:99] op_sel:[0,1] op_sel_hi:[1,1]
	v_pk_mul_f32 v[36:37], v[28:29], s[98:99] op_sel:[0,1] op_sel_hi:[1,1]
	v_pk_mul_f32 v[38:39], v[30:31], s[98:99] op_sel:[0,1] op_sel_hi:[1,1]
	v_pk_mul_f32 v[32:33], v[32:33], s[100:101] op_sel_hi:[1,0]
	v_pk_mul_f32 v[34:35], v[34:35], s[100:101] op_sel_hi:[1,0]
	v_pk_mul_f32 v[36:37], v[36:37], s[100:101] op_sel_hi:[1,0]
	v_pk_mul_f32 v[38:39], v[38:39], s[100:101] op_sel_hi:[1,0]
	v_pk_fma_f32 v[40:41], v[40:41], 4.0, 4.0 op_sel_hi:[1,0,0]
	v_pk_fma_f32 v[42:43], v[42:43], 4.0, 4.0 op_sel_hi:[1,0,0]
	v_pk_fma_f32 v[44:45], v[44:45], 4.0, 4.0 op_sel_hi:[1,0,0]
	v_pk_fma_f32 v[46:47], v[46:47], 4.0, 4.0 op_sel_hi:[1,0,0]
	v_exp_f32_e32 v32, v32
	v_exp_f32_e32 v33, v33
	v_exp_f32_e32 v34, v34
	v_exp_f32_e32 v35, v35
	v_exp_f32_e32 v36, v36
	v_exp_f32_e32 v37, v37
	v_exp_f32_e32 v38, v38
	v_exp_f32_e32 v39, v39
	v_pk_mul_f32 v[40:41], v[24:25], v[40:41]
	v_pk_mul_f32 v[42:43], v[26:27], v[42:43]
	v_pk_mul_f32 v[44:45], v[28:29], v[44:45]
	v_pk_mul_f32 v[46:47], v[30:31], v[46:47]
	v_pk_add_f32 v[32:33], v[32:33], 1.0 op_sel_hi:[1,0]
	v_pk_add_f32 v[34:35], v[34:35], 1.0 op_sel_hi:[1,0]
	v_pk_add_f32 v[36:37], v[36:37], 1.0 op_sel_hi:[1,0]
	v_pk_add_f32 v[38:39], v[38:39], 1.0 op_sel_hi:[1,0]
	v_rcp_f32_e32 v32, v32
	v_rcp_f32_e32 v33, v33
	v_rcp_f32_e32 v34, v34
	v_rcp_f32_e32 v35, v35
	v_rcp_f32_e32 v36, v36
	v_rcp_f32_e32 v37, v37
	v_rcp_f32_e32 v38, v38
	v_rcp_f32_e32 v39, v39
	v_pk_mul_f32 v[40:41], v[32:33], v[40:41]
	v_pk_mul_f32 v[42:43], v[34:35], v[42:43]
	v_pk_mul_f32 v[44:45], v[36:37], v[44:45]
	v_pk_mul_f32 v[46:47], v[38:39], v[46:47]
	v_cvt_pk_fp8_f32 v20, v40, v41
	v_cvt_pk_fp8_f32 v21, v44, v45
	v_cvt_pk_fp8_f32 v20, v42, v43 op_sel:[0,0,1]
	v_cvt_pk_fp8_f32 v21, v46, v47 op_sel:[0,0,1]
	v_pk_fma_f32 v[24:25], v[140:141], s[98:99], v[12:13] op_sel_hi:[1,0,1]
	v_pk_fma_f32 v[26:27], v[142:143], s[98:99], v[14:15] op_sel_hi:[1,0,1]
	v_pk_fma_f32 v[28:29], v[136:137], s[98:99], v[4:5] op_sel_hi:[1,0,1]
	v_pk_fma_f32 v[30:31], v[138:139], s[98:99], v[6:7] op_sel_hi:[1,0,1]
	v_pk_fma_f32 v[40:41], v[132:133], s[98:99], v[8:9] op_sel_hi:[1,0,1]
	v_pk_fma_f32 v[42:43], v[134:135], s[98:99], v[10:11] op_sel_hi:[1,0,1]
	v_pk_fma_f32 v[44:45], v[128:129], s[98:99], v[0:1] op_sel_hi:[1,0,1]
	v_pk_fma_f32 v[46:47], v[130:131], s[98:99], v[2:3] op_sel_hi:[1,0,1]
	v_min_f32_e32 v24, 0x40e00000, v24
	v_min_f32_e32 v25, 0x40e00000, v25
	v_min_f32_e32 v26, 0x40e00000, v26
	v_min_f32_e32 v27, 0x40e00000, v27
	v_min_f32_e32 v28, 0x40e00000, v28
	v_min_f32_e32 v29, 0x40e00000, v29
	v_min_f32_e32 v30, 0x40e00000, v30
; __device__ __forceinline__ unsigned pk4_fp8(float a, float b, float c, float d) { int w = __builtin_amdgcn_cvt_pk_fp8_f32(a, b, 0, false); w = __builtin_amdgcn_cvt_pk_fp8_f32(c, d, w, true); return (unsigned)w; }
;     __device__ __forceinline__ void operator()(const f32x4 (&acc)[2][2][4][2], const Unit& u, int wr, int wc, int fr, int fq) const {
;     ...
;                 for (int mi = 0; mi < 2; ++mi) { const int m = 2 * mp + mi;
;                     const f32x4 g0 = acc[ai][0][m][0] * ascale + bg0, g1 = acc[ai][0][m][1] * ascale + bg1, u0 = acc[ai][1][m][0] * ascale + bu0, u1 = acc[ai][1][m][1] * ascale + bu1;
;                     float r[8];
; #pragma unroll
;                     for (int j = 0; j < 4; ++j) {
;                         float gg = fminf(g0[j], 7.f), uu = fminf(fmaxf(u0[j], -7.f), 7.f); r[j] = 4.f * (uu + 1.f) * gg * __builtin_amdgcn_rcpf(1.f + __expf(-1.702f * gg));
;                         gg = fminf(g1[j], 7.f); uu = fminf(fmaxf(u1[j], -7.f), 7.f); r[4 + j] = 4.f * (uu + 1.f) * gg * __builtin_amdgcn_rcpf(1.f + __expf(-1.702f * gg));
;                     }
;                     wq[mi].x = pk4_fp8(r[0], r[1], r[2], r[3]); wq[mi].y = pk4_fp8(r[4], r[5], r[6], r[7]); }
;                 *(u32x4*)(act + (size_t)(row0 + ai * HALF + (2 * mp + (fq & 1)) * 16) * EFF + (c0 - 8 * (fq & 1))) = widen16(wq[0], wq[1]);
	v_min_f32_e32 v31, 0x40e00000, v31
	v_med3_f32 v40, v40, s74, v203
	v_med3_f32 v41, v41, s74, v203
	v_med3_f32 v42, v42, s74, v203
	v_med3_f32 v43, v43, s74, v203
	v_med3_f32 v44, v44, s74, v203
	v_med3_f32 v45, v45, s74, v203
	v_med3_f32 v46, v46, s74, v203
	v_med3_f32 v47, v47, s74, v203
	v_pk_mul_f32 v[32:33], v[24:25], s[98:99] op_sel:[0,1] op_sel_hi:[1,1]
	v_pk_mul_f32 v[34:35], v[26:27], s[98:99] op_sel:[0,1] op_sel_hi:[1,1]
	v_pk_mul_f32 v[36:37], v[28:29], s[98:99] op_sel:[0,1] op_sel_hi:[1,1]
	v_pk_mul_f32 v[38:39], v[30:31], s[98:99] op_sel:[0,1] op_sel_hi:[1,1]
	v_pk_mul_f32 v[32:33], v[32:33], s[100:101] op_sel_hi:[1,0]
	v_pk_mul_f32 v[34:35], v[34:35], s[100:101] op_sel_hi:[1,0]
	v_pk_mul_f32 v[36:37], v[36:37], s[100:101] op_sel_hi:[1,0]
	v_pk_mul_f32 v[38:39], v[38:39], s[100:101] op_sel_hi:[1,0]
	v_pk_fma_f32 v[40:41], v[40:41], 4.0, 4.0 op_sel_hi:[1,0,0]
	v_pk_fma_f32 v[42:43], v[42:43], 4.0, 4.0 op_sel_hi:[1,0,0]
	v_pk_fma_f32 v[44:45], v[44:45], 4.0, 4.0 op_sel_hi:[1,0,0]
	v_pk_fma_f32 v[46:47], v[46:47], 4.0, 4.0 op_sel_hi:[1,0,0]
	v_exp_f32_e32 v32, v32
	v_exp_f32_e32 v33, v33
	v_exp_f32_e32 v34, v34
	v_exp_f32_e32 v35, v35
	v_exp_f32_e32 v36, v36
	v_exp_f32_e32 v37, v37
	v_exp_f32_e32 v38, v38
	v_exp_f32_e32 v39, v39
	v_pk_mul_f32 v[40:41], v[24:25], v[40:41]
	v_pk_mul_f32 v[42:43], v[26:27], v[42:43]
	v_pk_mul_f32 v[44:45], v[28:29], v[44:45]
	v_pk_mul_f32 v[46:47], v[30:31], v[46:47]
	v_pk_add_f32 v[32:33], v[32:33], 1.0 op_sel_hi:[1,0]
	v_pk_add_f32 v[34:35], v[34:35], 1.0 op_sel_hi:[1,0]
	v_pk_add_f32 v[36:37], v[36:37], 1.0 op_sel_hi:[1,0]
	v_pk_add_f32 v[38:39], v[38:39], 1.0 op_sel_hi:[1,0]
	v_rcp_f32_e32 v32, v32
	v_rcp_f32_e32 v33, v33
	v_rcp_f32_e32 v34, v34
	v_rcp_f32_e32 v35, v35
	v_rcp_f32_e32 v36, v36
	v_rcp_f32_e32 v37, v37
	v_rcp_f32_e32 v38, v38
	v_rcp_f32_e32 v39, v39
	v_pk_mul_f32 v[40:41], v[32:33], v[40:41]
	v_pk_mul_f32 v[42:43], v[34:35], v[42:43]
	v_pk_mul_f32 v[44:45], v[36:37], v[44:45]
	v_pk_mul_f32 v[46:47], v[38:39], v[46:47]
	v_cvt_pk_fp8_f32 v22, v40, v41
	v_cvt_pk_fp8_f32 v23, v44, v45
	v_cvt_pk_fp8_f32 v22, v42, v43 op_sel:[0,0,1]
	v_cvt_pk_fp8_f32 v23, v46, v47 op_sel:[0,0,1]
	v_lshl_add_u64 v[50:51], v[48:49], 0, v[52:53]
	s_nop 1
	v_permlane16_swap_b32_e32 v20, v22
	v_permlane16_swap_b32_e32 v21, v23
	global_store_dwordx4 v[50:51], v[20:23], off
	v_pk_fma_f32 v[24:25], v[124:125], s[98:99], v[12:13] op_sel_hi:[1,0,1]
	v_pk_fma_f32 v[26:27], v[126:127], s[98:99], v[14:15] op_sel_hi:[1,0,1]
	v_pk_fma_f32 v[28:29], v[120:121], s[98:99], v[4:5] op_sel_hi:[1,0,1]
	v_pk_fma_f32 v[30:31], v[122:123], s[98:99], v[6:7] op_sel_hi:[1,0,1]
	v_pk_fma_f32 v[40:41], v[116:117], s[98:99], v[8:9] op_sel_hi:[1,0,1]
	v_pk_fma_f32 v[42:43], v[118:119], s[98:99], v[10:11] op_sel_hi:[1,0,1]
	v_pk_fma_f32 v[44:45], v[112:113], s[98:99], v[0:1] op_sel_hi:[1,0,1]
	v_pk_fma_f32 v[46:47], v[114:115], s[98:99], v[2:3] op_sel_hi:[1,0,1]
	v_min_f32_e32 v24, 0x40e00000, v24
	v_min_f32_e32 v25, 0x40e00000, v25
	v_min_f32_e32 v26, 0x40e00000, v26
	v_min_f32_e32 v27, 0x40e00000, v27
	v_min_f32_e32 v28, 0x40e00000, v28
	v_min_f32_e32 v29, 0x40e00000, v29
	v_min_f32_e32 v30, 0x40e00000, v30
	v_min_f32_e32 v31, 0x40e00000, v31
	v_med3_f32 v40, v40, s74, v203
	v_med3_f32 v41, v41, s74, v203
	v_med3_f32 v42, v42, s74, v203
	v_med3_f32 v43, v43, s74, v203
	v_med3_f32 v44, v44, s74, v203
	v_med3_f32 v45, v45, s74, v203
	v_med3_f32 v46, v46, s74, v203
	v_med3_f32 v47, v47, s74, v203
	v_pk_mul_f32 v[32:33], v[24:25], s[98:99] op_sel:[0,1] op_sel_hi:[1,1]
	v_pk_mul_f32 v[34:35], v[26:27], s[98:99] op_sel:[0,1] op_sel_hi:[1,1]
	v_pk_mul_f32 v[36:37], v[28:29], s[98:99] op_sel:[0,1] op_sel_hi:[1,1]
	v_pk_mul_f32 v[38:39], v[30:31], s[98:99] op_sel:[0,1] op_sel_hi:[1,1]
	v_pk_mul_f32 v[32:33], v[32:33], s[100:101] op_sel_hi:[1,0]
	v_pk_mul_f32 v[34:35], v[34:35], s[100:101] op_sel_hi:[1,0]
	v_pk_mul_f32 v[36:37], v[36:37], s[100:101] op_sel_hi:[1,0]
	v_pk_mul_f32 v[38:39], v[38:39], s[100:101] op_sel_hi:[1,0]
	v_pk_fma_f32 v[40:41], v[40:41], 4.0, 4.0 op_sel_hi:[1,0,0]
	v_pk_fma_f32 v[42:43], v[42:43], 4.0, 4.0 op_sel_hi:[1,0,0]
	v_pk_fma_f32 v[44:45], v[44:45], 4.0, 4.0 op_sel_hi:[1,0,0]
	v_pk_fma_f32 v[46:47], v[46:47], 4.0, 4.0 op_sel_hi:[1,0,0]
	v_exp_f32_e32 v32, v32
	v_exp_f32_e32 v33, v33
	v_exp_f32_e32 v34, v34
	v_exp_f32_e32 v35, v35
	v_exp_f32_e32 v36, v36
	v_exp_f32_e32 v37, v37
	v_exp_f32_e32 v38, v38
	v_exp_f32_e32 v39, v39
	v_pk_mul_f32 v[40:41], v[24:25], v[40:41]
	v_pk_mul_f32 v[42:43], v[26:27], v[42:43]
	v_pk_mul_f32 v[44:45], v[28:29], v[44:45]
	v_pk_mul_f32 v[46:47], v[30:31], v[46:47]
	v_pk_add_f32 v[32:33], v[32:33], 1.0 op_sel_hi:[1,0]
	v_pk_add_f32 v[34:35], v[34:35], 1.0 op_sel_hi:[1,0]
	v_pk_add_f32 v[36:37], v[36:37], 1.0 op_sel_hi:[1,0]
	v_pk_add_f32 v[38:39], v[38:39], 1.0 op_sel_hi:[1,0]
	v_rcp_f32_e32 v32, v32
	v_rcp_f32_e32 v33, v33
	v_rcp_f32_e32 v34, v34
	v_rcp_f32_e32 v35, v35
	v_rcp_f32_e32 v36, v36
	v_rcp_f32_e32 v37, v37
	v_rcp_f32_e32 v38, v38
	v_rcp_f32_e32 v39, v39
	v_pk_mul_f32 v[40:41], v[32:33], v[40:41]
	v_pk_mul_f32 v[42:43], v[34:35], v[42:43]
	v_pk_mul_f32 v[44:45], v[36:37], v[44:45]
	v_pk_mul_f32 v[46:47], v[38:39], v[46:47]
	v_cvt_pk_fp8_f32 v20, v40, v41
	v_cvt_pk_fp8_f32 v21, v44, v45
	v_cvt_pk_fp8_f32 v20, v42, v43 op_sel:[0,0,1]
	v_cvt_pk_fp8_f32 v21, v46, v47 op_sel:[0,0,1]
	v_pk_fma_f32 v[24:25], v[108:109], s[98:99], v[12:13] op_sel_hi:[1,0,1]
	v_pk_fma_f32 v[26:27], v[110:111], s[98:99], v[14:15] op_sel_hi:[1,0,1]
	v_pk_fma_f32 v[28:29], v[104:105], s[98:99], v[4:5] op_sel_hi:[1,0,1]
	v_pk_fma_f32 v[30:31], v[106:107], s[98:99], v[6:7] op_sel_hi:[1,0,1]
; __device__ __forceinline__ unsigned pk4_fp8(float a, float b, float c, float d) { int w = __builtin_amdgcn_cvt_pk_fp8_f32(a, b, 0, false); w = __builtin_amdgcn_cvt_pk_fp8_f32(c, d, w, true); return (unsigned)w; }
;     __device__ __forceinline__ void operator()(const f32x4 (&acc)[2][2][4][2], const Unit& u, int wr, int wc, int fr, int fq) const {
;     ...
;                 for (int mi = 0; mi < 2; ++mi) { const int m = 2 * mp + mi;
;                     const f32x4 g0 = acc[ai][0][m][0] * ascale + bg0, g1 = acc[ai][0][m][1] * ascale + bg1, u0 = acc[ai][1][m][0] * ascale + bu0, u1 = acc[ai][1][m][1] * ascale + bu1;
;                     float r[8];
; #pragma unroll
;                     for (int j = 0; j < 4; ++j) {
;                         float gg = fminf(g0[j], 7.f), uu = fminf(fmaxf(u0[j], -7.f), 7.f); r[j] = 4.f * (uu + 1.f) * gg * __builtin_amdgcn_rcpf(1.f + __expf(-1.702f * gg));
;                         gg = fminf(g1[j], 7.f); uu = fminf(fmaxf(u1[j], -7.f), 7.f); r[4 + j] = 4.f * (uu + 1.f) * gg * __builtin_amdgcn_rcpf(1.f + __expf(-1.702f * gg));
;                     }
;                     wq[mi].x = pk4_fp8(r[0], r[1], r[2], r[3]); wq[mi].y = pk4_fp8(r[4], r[5], r[6], r[7]); }
;                 *(u32x4*)(act + (size_t)(row0 + ai * HALF + (2 * mp + (fq & 1)) * 16) * EFF + (c0 - 8 * (fq & 1))) = widen16(wq[0], wq[1]);
	v_pk_fma_f32 v[40:41], v[100:101], s[98:99], v[8:9] op_sel_hi:[1,0,1]
	v_pk_fma_f32 v[42:43], v[102:103], s[98:99], v[10:11] op_sel_hi:[1,0,1]
	v_pk_fma_f32 v[44:45], v[96:97], s[98:99], v[0:1] op_sel_hi:[1,0,1]
	v_pk_fma_f32 v[46:47], v[98:99], s[98:99], v[2:3] op_sel_hi:[1,0,1]
	v_min_f32_e32 v24, 0x40e00000, v24
	v_min_f32_e32 v25, 0x40e00000, v25
	v_min_f32_e32 v26, 0x40e00000, v26
	v_min_f32_e32 v27, 0x40e00000, v27
	v_min_f32_e32 v28, 0x40e00000, v28
	v_min_f32_e32 v29, 0x40e00000, v29
	v_min_f32_e32 v30, 0x40e00000, v30
	v_min_f32_e32 v31, 0x40e00000, v31
	v_med3_f32 v40, v40, s74, v203
	v_med3_f32 v41, v41, s74, v203
	v_med3_f32 v42, v42, s74, v203
	v_med3_f32 v43, v43, s74, v203
	v_med3_f32 v44, v44, s74, v203
	v_med3_f32 v45, v45, s74, v203
	v_med3_f32 v46, v46, s74, v203
	v_med3_f32 v47, v47, s74, v203
	v_pk_mul_f32 v[32:33], v[24:25], s[98:99] op_sel:[0,1] op_sel_hi:[1,1]
	v_pk_mul_f32 v[34:35], v[26:27], s[98:99] op_sel:[0,1] op_sel_hi:[1,1]
	v_pk_mul_f32 v[36:37], v[28:29], s[98:99] op_sel:[0,1] op_sel_hi:[1,1]
	v_pk_mul_f32 v[38:39], v[30:31], s[98:99] op_sel:[0,1] op_sel_hi:[1,1]
	v_pk_mul_f32 v[32:33], v[32:33], s[100:101] op_sel_hi:[1,0]
	v_pk_mul_f32 v[34:35], v[34:35], s[100:101] op_sel_hi:[1,0]
	v_pk_mul_f32 v[36:37], v[36:37], s[100:101] op_sel_hi:[1,0]
	v_pk_mul_f32 v[38:39], v[38:39], s[100:101] op_sel_hi:[1,0]
	v_pk_fma_f32 v[40:41], v[40:41], 4.0, 4.0 op_sel_hi:[1,0,0]
	v_pk_fma_f32 v[42:43], v[42:43], 4.0, 4.0 op_sel_hi:[1,0,0]
	v_pk_fma_f32 v[44:45], v[44:45], 4.0, 4.0 op_sel_hi:[1,0,0]
	v_pk_fma_f32 v[46:47], v[46:47], 4.0, 4.0 op_sel_hi:[1,0,0]
	v_exp_f32_e32 v32, v32
	v_exp_f32_e32 v33, v33
	v_exp_f32_e32 v34, v34
	v_exp_f32_e32 v35, v35
	v_exp_f32_e32 v36, v36
	v_exp_f32_e32 v37, v37
	v_exp_f32_e32 v38, v38
	v_exp_f32_e32 v39, v39
	v_pk_mul_f32 v[40:41], v[24:25], v[40:41]
	v_pk_mul_f32 v[42:43], v[26:27], v[42:43]
	v_pk_mul_f32 v[44:45], v[28:29], v[44:45]
	v_pk_mul_f32 v[46:47], v[30:31], v[46:47]
	v_pk_add_f32 v[32:33], v[32:33], 1.0 op_sel_hi:[1,0]
	v_pk_add_f32 v[34:35], v[34:35], 1.0 op_sel_hi:[1,0]
	v_pk_add_f32 v[36:37], v[36:37], 1.0 op_sel_hi:[1,0]
	v_pk_add_f32 v[38:39], v[38:39], 1.0 op_sel_hi:[1,0]
	v_rcp_f32_e32 v32, v32
	v_rcp_f32_e32 v33, v33
	v_rcp_f32_e32 v34, v34
	v_rcp_f32_e32 v35, v35
	v_rcp_f32_e32 v36, v36
	v_rcp_f32_e32 v37, v37
	v_rcp_f32_e32 v38, v38
	v_rcp_f32_e32 v39, v39
	v_pk_mul_f32 v[40:41], v[32:33], v[40:41]
	v_pk_mul_f32 v[42:43], v[34:35], v[42:43]
	v_pk_mul_f32 v[44:45], v[36:37], v[44:45]
	v_pk_mul_f32 v[46:47], v[38:39], v[46:47]
	v_cvt_pk_fp8_f32 v22, v40, v41
	v_cvt_pk_fp8_f32 v23, v44, v45
	v_cvt_pk_fp8_f32 v22, v42, v43 op_sel:[0,0,1]
	v_cvt_pk_fp8_f32 v23, v46, v47 op_sel:[0,0,1]
	v_lshl_add_u64 v[50:51], v[48:49], 0, v[54:55]
	s_nop 1
	v_permlane16_swap_b32_e32 v20, v22
	v_permlane16_swap_b32_e32 v21, v23
	global_store_dwordx4 v[50:51], v[20:23], off
	v_pk_fma_f32 v[24:25], v[92:93], s[98:99], v[12:13] op_sel_hi:[1,0,1]
	v_pk_fma_f32 v[26:27], v[94:95], s[98:99], v[14:15] op_sel_hi:[1,0,1]
	v_pk_fma_f32 v[28:29], v[88:89], s[98:99], v[4:5] op_sel_hi:[1,0,1]
	v_pk_fma_f32 v[30:31], v[90:91], s[98:99], v[6:7] op_sel_hi:[1,0,1]
	v_pk_fma_f32 v[40:41], v[84:85], s[98:99], v[8:9] op_sel_hi:[1,0,1]
	v_pk_fma_f32 v[42:43], v[86:87], s[98:99], v[10:11] op_sel_hi:[1,0,1]
	v_pk_fma_f32 v[44:45], v[80:81], s[98:99], v[0:1] op_sel_hi:[1,0,1]
	v_pk_fma_f32 v[46:47], v[82:83], s[98:99], v[2:3] op_sel_hi:[1,0,1]
	v_min_f32_e32 v24, 0x40e00000, v24
	v_min_f32_e32 v25, 0x40e00000, v25
	v_min_f32_e32 v26, 0x40e00000, v26
	v_min_f32_e32 v27, 0x40e00000, v27
	v_min_f32_e32 v28, 0x40e00000, v28
	v_min_f32_e32 v29, 0x40e00000, v29
	v_min_f32_e32 v30, 0x40e00000, v30
	v_min_f32_e32 v31, 0x40e00000, v31
	v_med3_f32 v40, v40, s74, v203
	v_med3_f32 v41, v41, s74, v203
	v_med3_f32 v42, v42, s74, v203
	v_med3_f32 v43, v43, s74, v203
	v_med3_f32 v44, v44, s74, v203
	v_med3_f32 v45, v45, s74, v203
	v_med3_f32 v46, v46, s74, v203
	v_med3_f32 v47, v47, s74, v203
	v_pk_mul_f32 v[32:33], v[24:25], s[98:99] op_sel:[0,1] op_sel_hi:[1,1]
	v_pk_mul_f32 v[34:35], v[26:27], s[98:99] op_sel:[0,1] op_sel_hi:[1,1]
	v_pk_mul_f32 v[36:37], v[28:29], s[98:99] op_sel:[0,1] op_sel_hi:[1,1]
	v_pk_mul_f32 v[38:39], v[30:31], s[98:99] op_sel:[0,1] op_sel_hi:[1,1]
	v_pk_mul_f32 v[32:33], v[32:33], s[100:101] op_sel_hi:[1,0]
	v_pk_mul_f32 v[34:35], v[34:35], s[100:101] op_sel_hi:[1,0]
	v_pk_mul_f32 v[36:37], v[36:37], s[100:101] op_sel_hi:[1,0]
	v_pk_mul_f32 v[38:39], v[38:39], s[100:101] op_sel_hi:[1,0]
	v_pk_fma_f32 v[40:41], v[40:41], 4.0, 4.0 op_sel_hi:[1,0,0]
; #define PG8_BAR __builtin_amdgcn_s_barrier()
; __device__ __forceinline__ unsigned pk4_fp8(float a, float b, float c, float d) { int w = __builtin_amdgcn_cvt_pk_fp8_f32(a, b, 0, false); w = __builtin_amdgcn_cvt_pk_fp8_f32(c, d, w, true); return (unsigned)w; }
; template <class Epi, class Sched, bool ALIGN_EPI = true, bool SP2 = true, bool FP8 = false, bool GATHER = false>
; __device__ __forceinline__ void gemm_phase(LAS unsigned char* lds, const Dims g, const Sched& S, const Epi& E, const int wv) {
;     ...
;         if (!has_next) break;
; #pragma unroll
;         for (int a = 0; a < 2; ++a)
; #pragma unroll
;             for (int b = 0; b < 2; ++b)
; #pragma unroll
;                 for (int m = 0; m < 4; ++m)
; #pragma unroll
;                     for (int n = 0; n < 2; ++n) acc[a][b][m][n] = (f32x4){0.f, 0.f, 0.f, 0.f};
;         cur = nxt; cA = nA; cB = nB; ++ui;
;         if constexpr (ALIGN_EPI) { if (wr == 1) PG8_BAR; }
;     __device__ __forceinline__ void operator()(const f32x4 (&acc)[2][2][4][2], const Unit& u, int wr, int wc, int fr, int fq) const {
;     ...
;                 for (int mi = 0; mi < 2; ++mi) { const int m = 2 * mp + mi;
;                     const f32x4 g0 = acc[ai][0][m][0] * ascale + bg0, g1 = acc[ai][0][m][1] * ascale + bg1, u0 = acc[ai][1][m][0] * ascale + bu0, u1 = acc[ai][1][m][1] * ascale + bu1;
;                     float r[8];
; #pragma unroll
;                     for (int j = 0; j < 4; ++j) {
;                         float gg = fminf(g0[j], 7.f), uu = fminf(fmaxf(u0[j], -7.f), 7.f); r[j] = 4.f * (uu + 1.f) * gg * __builtin_amdgcn_rcpf(1.f + __expf(-1.702f * gg));
;                         gg = fminf(g1[j], 7.f); uu = fminf(fmaxf(u1[j], -7.f), 7.f); r[4 + j] = 4.f * (uu + 1.f) * gg * __builtin_amdgcn_rcpf(1.f + __expf(-1.702f * gg));
;                     }
;                     wq[mi].x = pk4_fp8(r[0], r[1], r[2], r[3]); wq[mi].y = pk4_fp8(r[4], r[5], r[6], r[7]); }
;                 *(u32x4*)(act + (size_t)(row0 + ai * HALF + (2 * mp + (fq & 1)) * 16) * EFF + (c0 - 8 * (fq & 1))) = widen16(wq[0], wq[1]);
;             }
	v_pk_fma_f32 v[42:43], v[42:43], 4.0, 4.0 op_sel_hi:[1,0,0]
	v_pk_fma_f32 v[44:45], v[44:45], 4.0, 4.0 op_sel_hi:[1,0,0]
	v_pk_fma_f32 v[46:47], v[46:47], 4.0, 4.0 op_sel_hi:[1,0,0]
	v_exp_f32_e32 v32, v32
	v_exp_f32_e32 v33, v33
	v_exp_f32_e32 v34, v34
	v_exp_f32_e32 v35, v35
	v_exp_f32_e32 v36, v36
	v_exp_f32_e32 v37, v37
	v_exp_f32_e32 v38, v38
	v_exp_f32_e32 v39, v39
	v_pk_mul_f32 v[40:41], v[24:25], v[40:41]
	v_pk_mul_f32 v[42:43], v[26:27], v[42:43]
	v_pk_mul_f32 v[44:45], v[28:29], v[44:45]
	v_pk_mul_f32 v[46:47], v[30:31], v[46:47]
	v_pk_add_f32 v[32:33], v[32:33], 1.0 op_sel_hi:[1,0]
	v_pk_add_f32 v[34:35], v[34:35], 1.0 op_sel_hi:[1,0]
	v_pk_add_f32 v[36:37], v[36:37], 1.0 op_sel_hi:[1,0]
	v_pk_add_f32 v[38:39], v[38:39], 1.0 op_sel_hi:[1,0]
	v_rcp_f32_e32 v32, v32
	v_rcp_f32_e32 v33, v33
	v_rcp_f32_e32 v34, v34
	v_rcp_f32_e32 v35, v35
	v_rcp_f32_e32 v36, v36
	v_rcp_f32_e32 v37, v37
	v_rcp_f32_e32 v38, v38
	v_rcp_f32_e32 v39, v39
	v_pk_mul_f32 v[40:41], v[32:33], v[40:41]
	v_pk_mul_f32 v[42:43], v[34:35], v[42:43]
	v_pk_mul_f32 v[44:45], v[36:37], v[44:45]
	v_pk_mul_f32 v[46:47], v[38:39], v[46:47]
	v_cvt_pk_fp8_f32 v20, v40, v41
	v_cvt_pk_fp8_f32 v21, v44, v45
	v_cvt_pk_fp8_f32 v20, v42, v43 op_sel:[0,0,1]
	v_cvt_pk_fp8_f32 v21, v46, v47 op_sel:[0,0,1]
	v_pk_fma_f32 v[24:25], v[76:77], s[98:99], v[12:13] op_sel_hi:[1,0,1]
	v_pk_fma_f32 v[26:27], v[78:79], s[98:99], v[14:15] op_sel_hi:[1,0,1]
	v_pk_fma_f32 v[28:29], v[72:73], s[98:99], v[4:5] op_sel_hi:[1,0,1]
	v_pk_fma_f32 v[30:31], v[74:75], s[98:99], v[6:7] op_sel_hi:[1,0,1]
	v_pk_fma_f32 v[40:41], v[68:69], s[98:99], v[8:9] op_sel_hi:[1,0,1]
	v_pk_fma_f32 v[42:43], v[70:71], s[98:99], v[10:11] op_sel_hi:[1,0,1]
	v_pk_fma_f32 v[44:45], v[64:65], s[98:99], v[0:1] op_sel_hi:[1,0,1]
	v_pk_fma_f32 v[46:47], v[66:67], s[98:99], v[2:3] op_sel_hi:[1,0,1]
	v_min_f32_e32 v24, 0x40e00000, v24
	v_min_f32_e32 v25, 0x40e00000, v25
	v_min_f32_e32 v26, 0x40e00000, v26
	v_min_f32_e32 v27, 0x40e00000, v27
	v_min_f32_e32 v28, 0x40e00000, v28
	v_min_f32_e32 v29, 0x40e00000, v29
	v_min_f32_e32 v30, 0x40e00000, v30
	v_min_f32_e32 v31, 0x40e00000, v31
	v_med3_f32 v40, v40, s74, v203
	v_med3_f32 v41, v41, s74, v203
	v_med3_f32 v42, v42, s74, v203
	v_med3_f32 v43, v43, s74, v203
	v_med3_f32 v44, v44, s74, v203
	v_med3_f32 v45, v45, s74, v203
	v_med3_f32 v46, v46, s74, v203
	v_med3_f32 v47, v47, s74, v203
	v_pk_mul_f32 v[32:33], v[24:25], s[98:99] op_sel:[0,1] op_sel_hi:[1,1]
	v_pk_mul_f32 v[34:35], v[26:27], s[98:99] op_sel:[0,1] op_sel_hi:[1,1]
	v_pk_mul_f32 v[36:37], v[28:29], s[98:99] op_sel:[0,1] op_sel_hi:[1,1]
	v_pk_mul_f32 v[38:39], v[30:31], s[98:99] op_sel:[0,1] op_sel_hi:[1,1]
	v_pk_mul_f32 v[32:33], v[32:33], s[100:101] op_sel_hi:[1,0]
	v_pk_mul_f32 v[34:35], v[34:35], s[100:101] op_sel_hi:[1,0]
	v_pk_mul_f32 v[36:37], v[36:37], s[100:101] op_sel_hi:[1,0]
	v_pk_mul_f32 v[38:39], v[38:39], s[100:101] op_sel_hi:[1,0]
	v_pk_fma_f32 v[40:41], v[40:41], 4.0, 4.0 op_sel_hi:[1,0,0]
	v_pk_fma_f32 v[42:43], v[42:43], 4.0, 4.0 op_sel_hi:[1,0,0]
	v_pk_fma_f32 v[44:45], v[44:45], 4.0, 4.0 op_sel_hi:[1,0,0]
	v_pk_fma_f32 v[46:47], v[46:47], 4.0, 4.0 op_sel_hi:[1,0,0]
	v_exp_f32_e32 v32, v32
	v_exp_f32_e32 v33, v33
	v_exp_f32_e32 v34, v34
	v_exp_f32_e32 v35, v35
	v_exp_f32_e32 v36, v36
	v_exp_f32_e32 v37, v37
	v_exp_f32_e32 v38, v38
	v_exp_f32_e32 v39, v39
	v_pk_mul_f32 v[40:41], v[24:25], v[40:41]
	v_pk_mul_f32 v[42:43], v[26:27], v[42:43]
	v_pk_mul_f32 v[44:45], v[28:29], v[44:45]
	v_pk_mul_f32 v[46:47], v[30:31], v[46:47]
	v_pk_add_f32 v[32:33], v[32:33], 1.0 op_sel_hi:[1,0]
	v_pk_add_f32 v[34:35], v[34:35], 1.0 op_sel_hi:[1,0]
	v_pk_add_f32 v[36:37], v[36:37], 1.0 op_sel_hi:[1,0]
	v_pk_add_f32 v[38:39], v[38:39], 1.0 op_sel_hi:[1,0]
	v_rcp_f32_e32 v32, v32
	v_rcp_f32_e32 v33, v33
	v_rcp_f32_e32 v34, v34
	v_rcp_f32_e32 v35, v35
	v_rcp_f32_e32 v36, v36
	v_rcp_f32_e32 v37, v37
	v_rcp_f32_e32 v38, v38
	v_rcp_f32_e32 v39, v39
	v_pk_mul_f32 v[40:41], v[32:33], v[40:41]
	v_pk_mul_f32 v[42:43], v[34:35], v[42:43]
	v_pk_mul_f32 v[44:45], v[36:37], v[44:45]
	v_pk_mul_f32 v[46:47], v[38:39], v[46:47]
	v_cvt_pk_fp8_f32 v22, v40, v41
	v_cvt_pk_fp8_f32 v23, v44, v45
	v_cvt_pk_fp8_f32 v22, v42, v43 op_sel:[0,0,1]
	v_cvt_pk_fp8_f32 v23, v46, v47 op_sel:[0,0,1]
	v_lshl_add_u64 v[50:51], v[48:49], 0, v[54:55]
	v_lshl_add_u64 v[50:51], v[50:51], 0, v[52:53]
	s_nop 1
	v_permlane16_swap_b32_e32 v20, v22
	v_permlane16_swap_b32_e32 v21, v23
	global_store_dwordx4 v[50:51], v[20:23], off
	s_cbranch_vccnz .LBB0_2523
	s_andn2_b64 vcc, exec, s[4:5]
	s_cbranch_vccnz .LBB0_2522
	s_barrier
	s_branch .LBB0_2522
